# v23 + GEMM K-loops: second K-step LDS-DMA addresses use the first K-step's address registers with offset:128 (M0 lowered by 128) instead of 16 64-bit VALU adds per trip
# baseline (speedup 1.0000x reference)
.LBB0_236:
	s_add_u32 s30, s28, 0xfff80080
	s_addc_u32 s31, s29, -1
	s_cmp_eq_u32 s75, 28
	s_cselect_b32 s35, s7, s31
	s_cselect_b32 s34, s21, s30
	s_cselect_b32 s31, s19, s74
	s_cselect_b32 s30, s72, s73
	v_lshl_add_u64 v[206:207], s[28:29], 0, v[138:139]
	s_add_i32 m0, s9, 0xc000
	ds_read_b128 v[172:175], v157
	ds_read_b128 v[176:179], v157 offset:1024
	ds_read_b128 v[180:183], v157 offset:2048
	ds_read_b128 v[184:187], v157 offset:3072
	ds_read_b128 v[188:191], v157 offset:4096
	ds_read_b128 v[192:195], v157 offset:5120
	ds_read_b128 v[198:201], v157 offset:6144
	ds_read_b128 v[202:205], v157 offset:7168
	global_load_lds_dwordx4 v[206:207], off
	v_lshl_add_u64 v[206:207], s[28:29], 0, v[140:141]
	s_add_i32 m0, s9, 0xe000
	s_nop 0
	global_load_lds_dwordx4 v[206:207], off
	s_waitcnt lgkmcnt(8)
	s_barrier
	s_waitcnt lgkmcnt(0)
	s_waitcnt lgkmcnt(0)
	v_mfma_f32_16x16x32_bf16 v[126:129], v[146:149], v[172:175], v[126:129]
	v_mfma_f32_16x16x32_bf16 v[122:125], v[164:167], v[172:175], v[122:125]
	v_mfma_f32_16x16x32_bf16 v[110:113], v[146:149], v[180:183], v[110:113]
	v_mfma_f32_16x16x32_bf16 v[106:109], v[164:167], v[180:183], v[106:109]
	v_mfma_f32_16x16x32_bf16 v[94:97], v[146:149], v[188:191], v[94:97]
	v_mfma_f32_16x16x32_bf16 v[90:93], v[164:167], v[188:191], v[90:93]
	v_mfma_f32_16x16x32_bf16 v[78:81], v[146:149], v[198:201], v[78:81]
	v_mfma_f32_16x16x32_bf16 v[74:77], v[164:167], v[198:201], v[74:77]
	v_mfma_f32_16x16x32_bf16 v[126:129], v[160:163], v[176:179], v[126:129]
	v_mfma_f32_16x16x32_bf16 v[122:125], v[168:171], v[176:179], v[122:125]
	v_mfma_f32_16x16x32_bf16 v[110:113], v[160:163], v[184:187], v[110:113]
	v_mfma_f32_16x16x32_bf16 v[106:109], v[168:171], v[184:187], v[106:109]
	v_mfma_f32_16x16x32_bf16 v[94:97], v[160:163], v[192:195], v[94:97]
	v_mfma_f32_16x16x32_bf16 v[90:93], v[168:171], v[192:195], v[90:93]
	v_mfma_f32_16x16x32_bf16 v[78:81], v[160:163], v[202:205], v[78:81]
	v_mfma_f32_16x16x32_bf16 v[74:77], v[168:171], v[202:205], v[74:77]
	s_barrier
	s_add_i32 s76, s69, s40
	v_lshl_add_u64 v[222:223], s[30:31], 0, v[132:133]
	s_mov_b32 m0, s76
	ds_read_b128 v[206:209], v158
	ds_read_b128 v[210:213], v158 offset:1024
	ds_read_b128 v[214:217], v158 offset:2048
	ds_read_b128 v[218:221], v158 offset:3072
	global_load_lds_dwordx4 v[222:223], off
	v_lshl_add_u64 v[224:225], s[30:31], 0, v[136:137]
	s_add_i32 m0, s76, 0x2000
	s_nop 0
	global_load_lds_dwordx4 v[224:225], off
	s_barrier
	s_waitcnt lgkmcnt(0)
	s_waitcnt lgkmcnt(0)
	v_mfma_f32_16x16x32_bf16 v[118:121], v[206:209], v[172:175], v[118:121]
	v_mfma_f32_16x16x32_bf16 v[114:117], v[214:217], v[172:175], v[114:117]
	v_mfma_f32_16x16x32_bf16 v[102:105], v[206:209], v[180:183], v[102:105]
	v_mfma_f32_16x16x32_bf16 v[98:101], v[214:217], v[180:183], v[98:101]
	v_mfma_f32_16x16x32_bf16 v[86:89], v[206:209], v[188:191], v[86:89]
	v_mfma_f32_16x16x32_bf16 v[82:85], v[214:217], v[188:191], v[82:85]
	v_mfma_f32_16x16x32_bf16 v[70:73], v[206:209], v[198:201], v[70:73]
	v_mfma_f32_16x16x32_bf16 v[66:69], v[214:217], v[198:201], v[66:69]
	v_mfma_f32_16x16x32_bf16 v[118:121], v[210:213], v[176:179], v[118:121]
	v_mfma_f32_16x16x32_bf16 v[114:117], v[218:221], v[176:179], v[114:117]
	v_mfma_f32_16x16x32_bf16 v[102:105], v[210:213], v[184:187], v[102:105]
	v_mfma_f32_16x16x32_bf16 v[98:101], v[218:221], v[184:187], v[98:101]
	v_mfma_f32_16x16x32_bf16 v[86:89], v[210:213], v[192:195], v[86:89]
	v_mfma_f32_16x16x32_bf16 v[82:85], v[218:221], v[192:195], v[82:85]
	v_mfma_f32_16x16x32_bf16 v[70:73], v[210:213], v[202:205], v[70:73]
	v_mfma_f32_16x16x32_bf16 v[66:69], v[218:221], v[202:205], v[66:69]
	s_mov_b32 m0, s9
	v_lshl_add_u64 v[226:227], s[34:35], 0, v[130:131]
	s_barrier
	ds_read_b128 v[172:175], v157 offset:16384
	ds_read_b128 v[176:179], v157 offset:17408
	ds_read_b128 v[180:183], v157 offset:18432
	ds_read_b128 v[184:187], v157 offset:19456
	ds_read_b128 v[188:191], v157 offset:20480
	ds_read_b128 v[192:195], v157 offset:21504
	ds_read_b128 v[198:201], v157 offset:22528
	ds_read_b128 v[202:205], v157 offset:23552
	global_load_lds_dwordx4 v[226:227], off
	v_lshl_add_u64 v[228:229], s[34:35], 0, v[134:135]
	s_mov_b32 m0, s53
	s_nop 0
	global_load_lds_dwordx4 v[228:229], off
	s_waitcnt vmcnt(10)
	s_barrier
	s_waitcnt lgkmcnt(0)
	s_waitcnt lgkmcnt(0)
	v_mfma_f32_16x16x32_bf16 v[62:65], v[146:149], v[172:175], v[62:65]
	v_mfma_f32_16x16x32_bf16 v[58:61], v[164:167], v[172:175], v[58:61]
	v_mfma_f32_16x16x32_bf16 v[46:49], v[146:149], v[180:183], v[46:49]
	v_mfma_f32_16x16x32_bf16 v[42:45], v[164:167], v[180:183], v[42:45]
	v_mfma_f32_16x16x32_bf16 v[30:33], v[146:149], v[188:191], v[30:33]
	v_mfma_f32_16x16x32_bf16 v[26:29], v[164:167], v[188:191], v[26:29]
	v_mfma_f32_16x16x32_bf16 v[14:17], v[146:149], v[198:201], v[14:17]
	v_mfma_f32_16x16x32_bf16 v[10:13], v[164:167], v[198:201], v[10:13]
	v_mfma_f32_16x16x32_bf16 v[62:65], v[160:163], v[176:179], v[62:65]
	v_mfma_f32_16x16x32_bf16 v[58:61], v[168:171], v[176:179], v[58:61]
	v_mfma_f32_16x16x32_bf16 v[46:49], v[160:163], v[184:187], v[46:49]
	v_mfma_f32_16x16x32_bf16 v[42:45], v[168:171], v[184:187], v[42:45]
	v_mfma_f32_16x16x32_bf16 v[30:33], v[160:163], v[192:195], v[30:33]
	v_mfma_f32_16x16x32_bf16 v[26:29], v[168:171], v[192:195], v[26:29]
	v_mfma_f32_16x16x32_bf16 v[14:17], v[160:163], v[202:205], v[14:17]
	v_mfma_f32_16x16x32_bf16 v[10:13], v[168:171], v[202:205], v[10:13]
	s_barrier
	ds_read_b128 v[146:149], v156 offset:32768
	ds_read_b128 v[160:163], v156 offset:33792
	ds_read_b128 v[164:167], v156 offset:34816
	ds_read_b128 v[168:171], v156 offset:35840
	s_add_u32 s76, s30, 0x80000
	s_addc_u32 s77, s31, 0
	s_add_i32 s78, s70, s40
	v_lshl_add_u64 v[230:231], s[76:77], 0, v[132:133]
	s_mov_b32 m0, s78
	s_nop 0
	global_load_lds_dwordx4 v[230:231], off
	v_lshl_add_u64 v[230:231], s[76:77], 0, v[136:137]
	s_add_i32 m0, s78, 0x2000
	s_nop 0
	global_load_lds_dwordx4 v[230:231], off
	s_waitcnt vmcnt(6)
	s_barrier
	v_mfma_f32_16x16x32_bf16 v[54:57], v[206:209], v[172:175], v[54:57]
	v_mfma_f32_16x16x32_bf16 v[50:53], v[214:217], v[172:175], v[50:53]
	v_mfma_f32_16x16x32_bf16 v[38:41], v[206:209], v[180:183], v[38:41]
	v_mfma_f32_16x16x32_bf16 v[34:37], v[214:217], v[180:183], v[34:37]
	v_mfma_f32_16x16x32_bf16 v[22:25], v[206:209], v[188:191], v[22:25]
	v_mfma_f32_16x16x32_bf16 v[18:21], v[214:217], v[188:191], v[18:21]
	v_mfma_f32_16x16x32_bf16 v[6:9], v[206:209], v[198:201], v[6:9]
	v_mfma_f32_16x16x32_bf16 v[2:5], v[214:217], v[198:201], v[2:5]
	v_mfma_f32_16x16x32_bf16 v[54:57], v[210:213], v[176:179], v[54:57]
	v_mfma_f32_16x16x32_bf16 v[50:53], v[218:221], v[176:179], v[50:53]
	v_mfma_f32_16x16x32_bf16 v[38:41], v[210:213], v[184:187], v[38:41]
	v_mfma_f32_16x16x32_bf16 v[34:37], v[218:221], v[184:187], v[34:37]
	v_mfma_f32_16x16x32_bf16 v[22:25], v[210:213], v[192:195], v[22:25]
	v_mfma_f32_16x16x32_bf16 v[18:21], v[218:221], v[192:195], v[18:21]
	v_mfma_f32_16x16x32_bf16 v[6:9], v[210:213], v[202:205], v[6:9]
	v_mfma_f32_16x16x32_bf16 v[2:5], v[218:221], v[202:205], v[2:5]
	s_add_i32 s76, 0, 0x18000
	v_add_u32_e32 v159, s76, v153
	s_barrier
	s_add_u32 s34, s34, 0x80000
	s_addc_u32 s35, s35, 0
	s_mov_b32 m0, s54
	v_lshl_add_u64 v[206:207], s[34:35], 0, v[130:131]
	ds_read_b128 v[172:175], v157 offset:32768
	ds_read_b128 v[176:179], v157 offset:33792
	ds_read_b128 v[180:183], v157 offset:34816
	ds_read_b128 v[184:187], v157 offset:35840
	ds_read_b128 v[188:191], v157 offset:36864
	ds_read_b128 v[192:195], v157 offset:37888
	ds_read_b128 v[198:201], v157 offset:38912
	ds_read_b128 v[202:205], v157 offset:39936
	global_load_lds_dwordx4 v[206:207], off
	v_lshl_add_u64 v[206:207], s[34:35], 0, v[134:135]
	s_mov_b32 m0, s55
	s_nop 0
	global_load_lds_dwordx4 v[206:207], off
	s_waitcnt lgkmcnt(8)
	s_barrier
	s_waitcnt lgkmcnt(0)
	s_waitcnt lgkmcnt(0)
	v_mfma_f32_16x16x32_bf16 v[126:129], v[146:149], v[172:175], v[126:129]
	v_mfma_f32_16x16x32_bf16 v[122:125], v[164:167], v[172:175], v[122:125]
	v_mfma_f32_16x16x32_bf16 v[110:113], v[146:149], v[180:183], v[110:113]
	v_mfma_f32_16x16x32_bf16 v[106:109], v[164:167], v[180:183], v[106:109]
	v_mfma_f32_16x16x32_bf16 v[94:97], v[146:149], v[188:191], v[94:97]
	v_mfma_f32_16x16x32_bf16 v[90:93], v[164:167], v[188:191], v[90:93]
	v_mfma_f32_16x16x32_bf16 v[78:81], v[146:149], v[198:201], v[78:81]
	v_mfma_f32_16x16x32_bf16 v[74:77], v[164:167], v[198:201], v[74:77]
	v_mfma_f32_16x16x32_bf16 v[126:129], v[160:163], v[176:179], v[126:129]
	v_mfma_f32_16x16x32_bf16 v[122:125], v[168:171], v[176:179], v[122:125]
	v_mfma_f32_16x16x32_bf16 v[110:113], v[160:163], v[184:187], v[110:113]
	v_mfma_f32_16x16x32_bf16 v[106:109], v[168:171], v[184:187], v[106:109]
	v_mfma_f32_16x16x32_bf16 v[94:97], v[160:163], v[192:195], v[94:97]
	v_mfma_f32_16x16x32_bf16 v[90:93], v[168:171], v[192:195], v[90:93]
	v_mfma_f32_16x16x32_bf16 v[78:81], v[160:163], v[202:205], v[78:81]
	v_mfma_f32_16x16x32_bf16 v[74:77], v[168:171], v[202:205], v[74:77]
	s_barrier
	s_add_i32 s34, 0, 0x1c000
	s_add_i32 s35, s76, s40
	v_add_u32_e32 v159, s34, v153
	s_add_i32 m0, s35, 0xffffff80
	ds_read_b128 v[206:209], v159
	ds_read_b128 v[210:213], v159 offset:1024
	ds_read_b128 v[214:217], v159 offset:2048
	ds_read_b128 v[218:221], v159 offset:3072
	global_load_lds_dwordx4 v[222:223], off offset:128
	s_add_i32 m0, s35, 0x1f80
	s_nop 0
	global_load_lds_dwordx4 v[224:225], off offset:128
	s_barrier
	s_waitcnt lgkmcnt(0)
	s_waitcnt lgkmcnt(0)
	v_mfma_f32_16x16x32_bf16 v[118:121], v[206:209], v[172:175], v[118:121]
	v_mfma_f32_16x16x32_bf16 v[114:117], v[214:217], v[172:175], v[114:117]
	v_mfma_f32_16x16x32_bf16 v[102:105], v[206:209], v[180:183], v[102:105]
	v_mfma_f32_16x16x32_bf16 v[98:101], v[214:217], v[180:183], v[98:101]
	v_mfma_f32_16x16x32_bf16 v[86:89], v[206:209], v[188:191], v[86:89]
	v_mfma_f32_16x16x32_bf16 v[82:85], v[214:217], v[188:191], v[82:85]
	v_mfma_f32_16x16x32_bf16 v[70:73], v[206:209], v[198:201], v[70:73]
	v_mfma_f32_16x16x32_bf16 v[66:69], v[214:217], v[198:201], v[66:69]
	v_mfma_f32_16x16x32_bf16 v[118:121], v[210:213], v[176:179], v[118:121]
	v_mfma_f32_16x16x32_bf16 v[114:117], v[218:221], v[176:179], v[114:117]
	v_mfma_f32_16x16x32_bf16 v[102:105], v[210:213], v[184:187], v[102:105]
	v_mfma_f32_16x16x32_bf16 v[98:101], v[218:221], v[184:187], v[98:101]
	v_mfma_f32_16x16x32_bf16 v[86:89], v[210:213], v[192:195], v[86:89]
	v_mfma_f32_16x16x32_bf16 v[82:85], v[218:221], v[192:195], v[82:85]
	v_mfma_f32_16x16x32_bf16 v[70:73], v[210:213], v[202:205], v[70:73]
	v_mfma_f32_16x16x32_bf16 v[66:69], v[218:221], v[202:205], v[66:69]
	s_add_i32 m0, s67, 0xffffff80
	s_barrier
	ds_read_b128 v[172:175], v157 offset:49152
	ds_read_b128 v[176:179], v157 offset:50176
	ds_read_b128 v[180:183], v157 offset:51200
	ds_read_b128 v[184:187], v157 offset:52224
	ds_read_b128 v[188:191], v157 offset:53248
	ds_read_b128 v[192:195], v157 offset:54272
	ds_read_b128 v[198:201], v157 offset:55296
	ds_read_b128 v[202:205], v157 offset:56320
	global_load_lds_dwordx4 v[226:227], off offset:128
	s_add_i32 m0, s68, 0xffffff80
	s_nop 0
	global_load_lds_dwordx4 v[228:229], off offset:128
	s_waitcnt vmcnt(10)
	s_barrier
	s_waitcnt lgkmcnt(0)
	s_waitcnt lgkmcnt(0)
	v_mfma_f32_16x16x32_bf16 v[62:65], v[146:149], v[172:175], v[62:65]
	v_mfma_f32_16x16x32_bf16 v[58:61], v[164:167], v[172:175], v[58:61]
	v_mfma_f32_16x16x32_bf16 v[46:49], v[146:149], v[180:183], v[46:49]
	v_mfma_f32_16x16x32_bf16 v[42:45], v[164:167], v[180:183], v[42:45]
	v_mfma_f32_16x16x32_bf16 v[30:33], v[146:149], v[188:191], v[30:33]
	v_mfma_f32_16x16x32_bf16 v[26:29], v[164:167], v[188:191], v[26:29]
	v_mfma_f32_16x16x32_bf16 v[14:17], v[146:149], v[198:201], v[14:17]
	v_mfma_f32_16x16x32_bf16 v[10:13], v[164:167], v[198:201], v[10:13]
	v_mfma_f32_16x16x32_bf16 v[62:65], v[160:163], v[176:179], v[62:65]
	v_mfma_f32_16x16x32_bf16 v[58:61], v[168:171], v[176:179], v[58:61]
	v_mfma_f32_16x16x32_bf16 v[46:49], v[160:163], v[184:187], v[46:49]
	v_mfma_f32_16x16x32_bf16 v[42:45], v[168:171], v[184:187], v[42:45]
	v_mfma_f32_16x16x32_bf16 v[30:33], v[160:163], v[192:195], v[30:33]
	v_mfma_f32_16x16x32_bf16 v[26:29], v[168:171], v[192:195], v[26:29]
	v_mfma_f32_16x16x32_bf16 v[14:17], v[160:163], v[202:205], v[14:17]
	v_mfma_f32_16x16x32_bf16 v[10:13], v[168:171], v[202:205], v[10:13]
	s_barrier
	ds_read_b128 v[146:149], v156
	ds_read_b128 v[160:163], v156 offset:1024
	ds_read_b128 v[164:167], v156 offset:2048
	ds_read_b128 v[168:171], v156 offset:3072
	s_add_u32 s30, s30, 0x80080
	s_addc_u32 s31, s31, 0
	s_add_i32 s34, s34, s40
	v_lshl_add_u64 v[230:231], s[30:31], 0, v[132:133]
	s_mov_b32 m0, s34
	s_nop 0
	global_load_lds_dwordx4 v[230:231], off
	v_lshl_add_u64 v[230:231], s[30:31], 0, v[136:137]
	s_add_i32 m0, s34, 0x2000
	s_nop 0
	global_load_lds_dwordx4 v[230:231], off
	s_waitcnt vmcnt(6)
	s_barrier
	v_mfma_f32_16x16x32_bf16 v[54:57], v[206:209], v[172:175], v[54:57]
	v_mfma_f32_16x16x32_bf16 v[50:53], v[214:217], v[172:175], v[50:53]
	v_mfma_f32_16x16x32_bf16 v[38:41], v[206:209], v[180:183], v[38:41]
	v_mfma_f32_16x16x32_bf16 v[34:37], v[214:217], v[180:183], v[34:37]
	v_mfma_f32_16x16x32_bf16 v[22:25], v[206:209], v[188:191], v[22:25]
	v_mfma_f32_16x16x32_bf16 v[18:21], v[214:217], v[188:191], v[18:21]
	v_mfma_f32_16x16x32_bf16 v[6:9], v[206:209], v[198:201], v[6:9]
	v_mfma_f32_16x16x32_bf16 v[2:5], v[214:217], v[198:201], v[2:5]
	v_mfma_f32_16x16x32_bf16 v[54:57], v[210:213], v[176:179], v[54:57]
	v_mfma_f32_16x16x32_bf16 v[50:53], v[218:221], v[176:179], v[50:53]
	v_mfma_f32_16x16x32_bf16 v[38:41], v[210:213], v[184:187], v[38:41]
	v_mfma_f32_16x16x32_bf16 v[34:37], v[218:221], v[184:187], v[34:37]
	v_mfma_f32_16x16x32_bf16 v[22:25], v[210:213], v[192:195], v[22:25]
	v_mfma_f32_16x16x32_bf16 v[18:21], v[218:221], v[192:195], v[18:21]
	v_mfma_f32_16x16x32_bf16 v[6:9], v[210:213], v[202:205], v[6:9]
	v_mfma_f32_16x16x32_bf16 v[2:5], v[218:221], v[202:205], v[2:5]
	s_add_i32 s75, s75, 2
	s_add_u32 s28, s28, 0x100
	s_addc_u32 s29, s29, 0
	s_add_u32 s73, s73, 0x100
	s_addc_u32 s74, s74, 0
	s_cmp_gt_u32 s75, 29
	s_barrier
	s_cbranch_scc0 .LBB0_236
	s_waitcnt lgkmcnt(0)
	s_add_i32 s7, s8, -12
	s_cmp_lt_u32 s7, 8
	v_lshl_add_u32 v159, s6, 8, v152
	s_cselect_b64 s[28:29], -1, 0
	s_cmp_lt_i32 s6, 64
	v_lshrrev_b32_e32 v160, 6, v159
	s_cselect_b64 s[30:31], -1, 0
	v_cndmask_b32_e64 v146, v151, v160, s[0:1]
	v_lshlrev_b32_e32 v146, 5, v146
	s_and_b64 s[28:29], s[28:29], s[30:31]
	v_and_b32_e32 v146, 0x7e0, v146
	v_cndmask_b32_e64 v147, 0, 1, s[28:29]
	v_cmp_ne_u32_e64 s[6:7], 1, v147
	s_andn2_b64 vcc, exec, s[28:29]
	v_lshl_add_u32 v161, v146, 2, v154
	s_cbranch_vccnz .LBB0_239
	ds_read_b128 v[146:149], v161
	ds_read_b128 v[162:165], v161 offset:16
	v_mov_b32_e32 v166, v129
	s_cmp_lt_u32 s8, 16
	s_cselect_b64 vcc, -1, 0
	s_waitcnt lgkmcnt(0)
	v_pk_mul_f32 v[168:169], v[126:127], v[146:147] op_sel:[1,1] op_sel_hi:[1,0]
	v_pk_mul_f32 v[166:167], v[166:167], v[148:149] op_sel:[0,1] op_sel_hi:[0,0]
	v_pk_fma_f32 v[170:171], v[126:127], v[146:147], v[168:169] op_sel_hi:[0,1,1] neg_lo:[0,0,1] neg_hi:[0,0,1]
	v_pk_fma_f32 v[126:127], v[126:127], v[146:147], v[168:169] op_sel_hi:[0,1,1]
	v_pk_fma_f32 v[146:147], v[128:129], v[148:149], v[166:167] op_sel_hi:[0,1,1] neg_lo:[0,0,1] neg_hi:[0,0,1]
	v_pk_fma_f32 v[128:129], v[128:129], v[148:149], v[166:167] op_sel_hi:[0,1,1]
	v_pk_mul_f32 v[148:149], v[122:123], v[162:163] op_sel:[1,1] op_sel_hi:[1,0]
	v_mov_b32_e32 v147, v129
	v_pk_fma_f32 v[166:167], v[122:123], v[162:163], v[148:149] op_sel_hi:[0,1,1] neg_lo:[0,0,1] neg_hi:[0,0,1]
	v_pk_fma_f32 v[122:123], v[122:123], v[162:163], v[148:149] op_sel_hi:[0,1,1]
	v_mov_b32_e32 v122, v125
	v_pk_mul_f32 v[148:149], v[122:123], v[164:165] op_sel:[0,1] op_sel_hi:[0,0]
	v_pk_fma_f32 v[162:163], v[124:125], v[164:165], v[148:149] op_sel_hi:[0,1,1] neg_lo:[0,0,1] neg_hi:[0,0,1]
	v_pk_fma_f32 v[124:125], v[124:125], v[164:165], v[148:149] op_sel_hi:[0,1,1]
	v_mov_b32_e32 v171, v127
	v_mov_b32_e32 v163, v125
	v_mov_b32_e32 v167, v123
	v_pk_mul_f32 v[148:149], v[146:147], s[16:17] op_sel_hi:[1,0]
	v_pk_mul_f32 v[164:165], v[170:171], s[16:17] op_sel_hi:[1,0]
	v_pk_mul_f32 v[168:169], v[162:163], s[16:17] op_sel_hi:[1,0]
	v_pk_mul_f32 v[172:173], v[166:167], s[16:17] op_sel_hi:[1,0]
	v_cndmask_b32_e32 v124, v162, v168, vcc
	v_cndmask_b32_e32 v125, v125, v169, vcc
	v_cndmask_b32_e32 v122, v166, v172, vcc
	v_cndmask_b32_e32 v123, v123, v173, vcc
	v_cndmask_b32_e32 v128, v146, v148, vcc
	v_cndmask_b32_e32 v129, v129, v149, vcc
	v_cndmask_b32_e32 v126, v170, v164, vcc
	v_cndmask_b32_e32 v127, v127, v165, vcc

.LBB0_715:
	s_add_u32 s30, s28, 0xfff80080
	s_addc_u32 s31, s29, -1
	s_cmp_eq_u32 s74, 28
	s_cselect_b32 s35, s21, s31
	s_cselect_b32 s34, s70, s30
	s_cselect_b32 s31, s19, s73
	s_cselect_b32 s30, s71, s72
	v_lshl_add_u64 v[146:147], s[28:29], 0, v[138:139]
	s_add_i32 m0, s27, 0xc000
	ds_read_b128 v[170:173], v151
	ds_read_b128 v[174:177], v151 offset:1024
	ds_read_b128 v[178:181], v151 offset:2048
	ds_read_b128 v[182:185], v151 offset:3072
	ds_read_b128 v[186:189], v151 offset:4096
	ds_read_b128 v[190:193], v151 offset:5120
	ds_read_b128 v[198:201], v151 offset:6144
	ds_read_b128 v[202:205], v151 offset:7168
	global_load_lds_dwordx4 v[146:147], off
	v_lshl_add_u64 v[146:147], s[28:29], 0, v[140:141]
	s_add_i32 m0, s27, 0xe000
	s_nop 0
	global_load_lds_dwordx4 v[146:147], off
	s_waitcnt lgkmcnt(8)
	s_barrier
	s_waitcnt lgkmcnt(0)
	s_waitcnt lgkmcnt(0)
	v_mfma_f32_16x16x32_bf16 v[126:129], v[154:157], v[170:173], v[126:129]
	v_mfma_f32_16x16x32_bf16 v[122:125], v[162:165], v[170:173], v[122:125]
	v_mfma_f32_16x16x32_bf16 v[114:117], v[154:157], v[178:181], v[114:117]
	v_mfma_f32_16x16x32_bf16 v[106:109], v[162:165], v[178:181], v[106:109]
	v_mfma_f32_16x16x32_bf16 v[98:101], v[154:157], v[186:189], v[98:101]
	v_mfma_f32_16x16x32_bf16 v[90:93], v[162:165], v[186:189], v[90:93]
	v_mfma_f32_16x16x32_bf16 v[82:85], v[154:157], v[198:201], v[82:85]
	v_mfma_f32_16x16x32_bf16 v[74:77], v[162:165], v[198:201], v[74:77]
	v_mfma_f32_16x16x32_bf16 v[126:129], v[158:161], v[174:177], v[126:129]
	v_mfma_f32_16x16x32_bf16 v[122:125], v[166:169], v[174:177], v[122:125]
	v_mfma_f32_16x16x32_bf16 v[114:117], v[158:161], v[182:185], v[114:117]
	v_mfma_f32_16x16x32_bf16 v[106:109], v[166:169], v[182:185], v[106:109]
	v_mfma_f32_16x16x32_bf16 v[98:101], v[158:161], v[190:193], v[98:101]
	v_mfma_f32_16x16x32_bf16 v[90:93], v[166:169], v[190:193], v[90:93]
	v_mfma_f32_16x16x32_bf16 v[82:85], v[158:161], v[202:205], v[82:85]
	v_mfma_f32_16x16x32_bf16 v[74:77], v[166:169], v[202:205], v[74:77]
	s_barrier
	s_add_i32 s75, s55, s40
	v_lshl_add_u64 v[146:147], s[30:31], 0, v[132:133]
	s_mov_b32 m0, s75
	ds_read_b128 v[206:209], v152
	ds_read_b128 v[210:213], v152 offset:1024
	ds_read_b128 v[214:217], v152 offset:2048
	ds_read_b128 v[218:221], v152 offset:3072
	global_load_lds_dwordx4 v[146:147], off
	v_lshl_add_u64 v[194:195], s[30:31], 0, v[136:137]
	s_add_i32 m0, s75, 0x2000
	s_nop 0
	global_load_lds_dwordx4 v[194:195], off
	s_barrier
	s_waitcnt lgkmcnt(0)
	s_waitcnt lgkmcnt(0)
	v_mfma_f32_16x16x32_bf16 v[118:121], v[206:209], v[170:173], v[118:121]
	v_mfma_f32_16x16x32_bf16 v[110:113], v[214:217], v[170:173], v[110:113]
	v_mfma_f32_16x16x32_bf16 v[102:105], v[206:209], v[178:181], v[102:105]
	v_mfma_f32_16x16x32_bf16 v[94:97], v[214:217], v[178:181], v[94:97]
	v_mfma_f32_16x16x32_bf16 v[86:89], v[206:209], v[186:189], v[86:89]
	v_mfma_f32_16x16x32_bf16 v[78:81], v[214:217], v[186:189], v[78:81]
	v_mfma_f32_16x16x32_bf16 v[70:73], v[206:209], v[198:201], v[70:73]
	v_mfma_f32_16x16x32_bf16 v[66:69], v[214:217], v[198:201], v[66:69]
	v_mfma_f32_16x16x32_bf16 v[118:121], v[210:213], v[174:177], v[118:121]
	v_mfma_f32_16x16x32_bf16 v[110:113], v[218:221], v[174:177], v[110:113]
	v_mfma_f32_16x16x32_bf16 v[102:105], v[210:213], v[182:185], v[102:105]
	v_mfma_f32_16x16x32_bf16 v[94:97], v[218:221], v[182:185], v[94:97]
	v_mfma_f32_16x16x32_bf16 v[86:89], v[210:213], v[190:193], v[86:89]
	v_mfma_f32_16x16x32_bf16 v[78:81], v[218:221], v[190:193], v[78:81]
	v_mfma_f32_16x16x32_bf16 v[70:73], v[210:213], v[202:205], v[70:73]
	v_mfma_f32_16x16x32_bf16 v[66:69], v[218:221], v[202:205], v[66:69]
	s_mov_b32 m0, s27
	v_lshl_add_u64 v[222:223], s[34:35], 0, v[130:131]
	s_barrier
	ds_read_b128 v[170:173], v151 offset:16384
	ds_read_b128 v[174:177], v151 offset:17408
	ds_read_b128 v[178:181], v151 offset:18432
	ds_read_b128 v[182:185], v151 offset:19456
	ds_read_b128 v[186:189], v151 offset:20480
	ds_read_b128 v[190:193], v151 offset:21504
	ds_read_b128 v[198:201], v151 offset:22528
	ds_read_b128 v[202:205], v151 offset:23552
	global_load_lds_dwordx4 v[222:223], off
	v_lshl_add_u64 v[224:225], s[34:35], 0, v[134:135]
	s_mov_b32 m0, s42
	s_nop 0
	global_load_lds_dwordx4 v[224:225], off
	s_waitcnt vmcnt(10)
	s_barrier
	s_waitcnt lgkmcnt(0)
	s_waitcnt lgkmcnt(0)
	v_mfma_f32_16x16x32_bf16 v[62:65], v[154:157], v[170:173], v[62:65]
	v_mfma_f32_16x16x32_bf16 v[58:61], v[162:165], v[170:173], v[58:61]
	v_mfma_f32_16x16x32_bf16 v[54:57], v[154:157], v[178:181], v[54:57]
	v_mfma_f32_16x16x32_bf16 v[46:49], v[162:165], v[178:181], v[46:49]
	v_mfma_f32_16x16x32_bf16 v[38:41], v[154:157], v[186:189], v[38:41]
	v_mfma_f32_16x16x32_bf16 v[30:33], v[162:165], v[186:189], v[30:33]
	v_mfma_f32_16x16x32_bf16 v[22:25], v[154:157], v[198:201], v[22:25]
	v_mfma_f32_16x16x32_bf16 v[14:17], v[162:165], v[198:201], v[14:17]
	v_mfma_f32_16x16x32_bf16 v[62:65], v[158:161], v[174:177], v[62:65]
	v_mfma_f32_16x16x32_bf16 v[58:61], v[166:169], v[174:177], v[58:61]
	v_mfma_f32_16x16x32_bf16 v[54:57], v[158:161], v[182:185], v[54:57]
	v_mfma_f32_16x16x32_bf16 v[46:49], v[166:169], v[182:185], v[46:49]
	v_mfma_f32_16x16x32_bf16 v[38:41], v[158:161], v[190:193], v[38:41]
	v_mfma_f32_16x16x32_bf16 v[30:33], v[166:169], v[190:193], v[30:33]
	v_mfma_f32_16x16x32_bf16 v[22:25], v[158:161], v[202:205], v[22:25]
	v_mfma_f32_16x16x32_bf16 v[14:17], v[166:169], v[202:205], v[14:17]
	s_barrier
	ds_read_b128 v[154:157], v150 offset:32768
	ds_read_b128 v[158:161], v150 offset:33792
	ds_read_b128 v[162:165], v150 offset:34816
	ds_read_b128 v[166:169], v150 offset:35840
	s_add_u32 s76, s30, 0x80000
	s_addc_u32 s77, s31, 0
	s_add_i32 s75, s64, s40
	v_lshl_add_u64 v[226:227], s[76:77], 0, v[132:133]
	s_mov_b32 m0, s75
	s_nop 0
	global_load_lds_dwordx4 v[226:227], off
	v_lshl_add_u64 v[226:227], s[76:77], 0, v[136:137]
	s_add_i32 m0, s75, 0x2000
	s_nop 0
	global_load_lds_dwordx4 v[226:227], off
	s_waitcnt vmcnt(6)
	s_barrier
	v_mfma_f32_16x16x32_bf16 v[50:53], v[206:209], v[170:173], v[50:53]
	v_mfma_f32_16x16x32_bf16 v[42:45], v[214:217], v[170:173], v[42:45]
	v_mfma_f32_16x16x32_bf16 v[34:37], v[206:209], v[178:181], v[34:37]
	v_mfma_f32_16x16x32_bf16 v[26:29], v[214:217], v[178:181], v[26:29]
	v_mfma_f32_16x16x32_bf16 v[18:21], v[206:209], v[186:189], v[18:21]
	v_mfma_f32_16x16x32_bf16 v[10:13], v[214:217], v[186:189], v[10:13]
	v_mfma_f32_16x16x32_bf16 v[6:9], v[206:209], v[198:201], v[6:9]
	v_mfma_f32_16x16x32_bf16 v[2:5], v[214:217], v[198:201], v[2:5]
	v_mfma_f32_16x16x32_bf16 v[50:53], v[210:213], v[174:177], v[50:53]
	v_mfma_f32_16x16x32_bf16 v[42:45], v[218:221], v[174:177], v[42:45]
	v_mfma_f32_16x16x32_bf16 v[34:37], v[210:213], v[182:185], v[34:37]
	v_mfma_f32_16x16x32_bf16 v[26:29], v[218:221], v[182:185], v[26:29]
	v_mfma_f32_16x16x32_bf16 v[18:21], v[210:213], v[190:193], v[18:21]
	v_mfma_f32_16x16x32_bf16 v[10:13], v[218:221], v[190:193], v[10:13]
	v_mfma_f32_16x16x32_bf16 v[6:9], v[210:213], v[202:205], v[6:9]
	v_mfma_f32_16x16x32_bf16 v[2:5], v[218:221], v[202:205], v[2:5]
	s_add_i32 s75, 0, 0x18000
	v_add_u32_e32 v153, s75, v148
	s_barrier
	s_add_u32 s34, s34, 0x80000
	s_addc_u32 s35, s35, 0
	s_mov_b32 m0, s43
	v_lshl_add_u64 v[206:207], s[34:35], 0, v[130:131]
	ds_read_b128 v[170:173], v151 offset:32768
	ds_read_b128 v[174:177], v151 offset:33792
	ds_read_b128 v[178:181], v151 offset:34816
	ds_read_b128 v[182:185], v151 offset:35840
	ds_read_b128 v[186:189], v151 offset:36864
	ds_read_b128 v[190:193], v151 offset:37888
	ds_read_b128 v[198:201], v151 offset:38912
	ds_read_b128 v[202:205], v151 offset:39936
	global_load_lds_dwordx4 v[206:207], off
	v_lshl_add_u64 v[206:207], s[34:35], 0, v[134:135]
	s_mov_b32 m0, s44
	s_nop 0
	global_load_lds_dwordx4 v[206:207], off
	s_waitcnt lgkmcnt(8)
	s_barrier
	s_waitcnt lgkmcnt(0)
	s_waitcnt lgkmcnt(0)
	v_mfma_f32_16x16x32_bf16 v[126:129], v[154:157], v[170:173], v[126:129]
	v_mfma_f32_16x16x32_bf16 v[122:125], v[162:165], v[170:173], v[122:125]
	v_mfma_f32_16x16x32_bf16 v[114:117], v[154:157], v[178:181], v[114:117]
	v_mfma_f32_16x16x32_bf16 v[106:109], v[162:165], v[178:181], v[106:109]
	v_mfma_f32_16x16x32_bf16 v[98:101], v[154:157], v[186:189], v[98:101]
	v_mfma_f32_16x16x32_bf16 v[90:93], v[162:165], v[186:189], v[90:93]
	v_mfma_f32_16x16x32_bf16 v[82:85], v[154:157], v[198:201], v[82:85]
	v_mfma_f32_16x16x32_bf16 v[74:77], v[162:165], v[198:201], v[74:77]
	v_mfma_f32_16x16x32_bf16 v[126:129], v[158:161], v[174:177], v[126:129]
	v_mfma_f32_16x16x32_bf16 v[122:125], v[166:169], v[174:177], v[122:125]
	v_mfma_f32_16x16x32_bf16 v[114:117], v[158:161], v[182:185], v[114:117]
	v_mfma_f32_16x16x32_bf16 v[106:109], v[166:169], v[182:185], v[106:109]
	v_mfma_f32_16x16x32_bf16 v[98:101], v[158:161], v[190:193], v[98:101]
	v_mfma_f32_16x16x32_bf16 v[90:93], v[166:169], v[190:193], v[90:93]
	v_mfma_f32_16x16x32_bf16 v[82:85], v[158:161], v[202:205], v[82:85]
	v_mfma_f32_16x16x32_bf16 v[74:77], v[166:169], v[202:205], v[74:77]
	s_barrier
	s_add_i32 s34, 0, 0x1c000
	s_add_i32 s35, s75, s40
	v_add_u32_e32 v153, s34, v148
	s_add_i32 m0, s35, 0xffffff80
	ds_read_b128 v[206:209], v153
	ds_read_b128 v[210:213], v153 offset:1024
	ds_read_b128 v[214:217], v153 offset:2048
	ds_read_b128 v[218:221], v153 offset:3072
	global_load_lds_dwordx4 v[146:147], off offset:128
	s_add_i32 m0, s35, 0x1f80
	s_nop 0
	global_load_lds_dwordx4 v[194:195], off offset:128
	s_barrier
	s_waitcnt lgkmcnt(0)
	s_waitcnt lgkmcnt(0)
	v_mfma_f32_16x16x32_bf16 v[118:121], v[206:209], v[170:173], v[118:121]
	v_mfma_f32_16x16x32_bf16 v[110:113], v[214:217], v[170:173], v[110:113]
	v_mfma_f32_16x16x32_bf16 v[102:105], v[206:209], v[178:181], v[102:105]
	v_mfma_f32_16x16x32_bf16 v[94:97], v[214:217], v[178:181], v[94:97]
	v_mfma_f32_16x16x32_bf16 v[86:89], v[206:209], v[186:189], v[86:89]
	v_mfma_f32_16x16x32_bf16 v[78:81], v[214:217], v[186:189], v[78:81]
	v_mfma_f32_16x16x32_bf16 v[70:73], v[206:209], v[198:201], v[70:73]
	v_mfma_f32_16x16x32_bf16 v[66:69], v[214:217], v[198:201], v[66:69]
	v_mfma_f32_16x16x32_bf16 v[118:121], v[210:213], v[174:177], v[118:121]
	v_mfma_f32_16x16x32_bf16 v[110:113], v[218:221], v[174:177], v[110:113]
	v_mfma_f32_16x16x32_bf16 v[102:105], v[210:213], v[182:185], v[102:105]
	v_mfma_f32_16x16x32_bf16 v[94:97], v[218:221], v[182:185], v[94:97]
	v_mfma_f32_16x16x32_bf16 v[86:89], v[210:213], v[190:193], v[86:89]
	v_mfma_f32_16x16x32_bf16 v[78:81], v[218:221], v[190:193], v[78:81]
	v_mfma_f32_16x16x32_bf16 v[70:73], v[210:213], v[202:205], v[70:73]
	v_mfma_f32_16x16x32_bf16 v[66:69], v[218:221], v[202:205], v[66:69]
	s_add_i32 m0, s53, 0xffffff80
	s_barrier
	ds_read_b128 v[170:173], v151 offset:49152
	ds_read_b128 v[174:177], v151 offset:50176
	ds_read_b128 v[178:181], v151 offset:51200
	ds_read_b128 v[182:185], v151 offset:52224
	ds_read_b128 v[186:189], v151 offset:53248
	ds_read_b128 v[190:193], v151 offset:54272
	ds_read_b128 v[198:201], v151 offset:55296
	ds_read_b128 v[202:205], v151 offset:56320
	global_load_lds_dwordx4 v[222:223], off offset:128
	s_add_i32 m0, s54, 0xffffff80
	s_nop 0
	global_load_lds_dwordx4 v[224:225], off offset:128
	s_waitcnt vmcnt(10)
	s_barrier
	s_waitcnt lgkmcnt(0)
	s_waitcnt lgkmcnt(0)
	v_mfma_f32_16x16x32_bf16 v[62:65], v[154:157], v[170:173], v[62:65]
	v_mfma_f32_16x16x32_bf16 v[58:61], v[162:165], v[170:173], v[58:61]
	v_mfma_f32_16x16x32_bf16 v[54:57], v[154:157], v[178:181], v[54:57]
	v_mfma_f32_16x16x32_bf16 v[46:49], v[162:165], v[178:181], v[46:49]
	v_mfma_f32_16x16x32_bf16 v[38:41], v[154:157], v[186:189], v[38:41]
	v_mfma_f32_16x16x32_bf16 v[30:33], v[162:165], v[186:189], v[30:33]
	v_mfma_f32_16x16x32_bf16 v[22:25], v[154:157], v[198:201], v[22:25]
	v_mfma_f32_16x16x32_bf16 v[14:17], v[162:165], v[198:201], v[14:17]
	v_mfma_f32_16x16x32_bf16 v[62:65], v[158:161], v[174:177], v[62:65]
	v_mfma_f32_16x16x32_bf16 v[58:61], v[166:169], v[174:177], v[58:61]
	v_mfma_f32_16x16x32_bf16 v[54:57], v[158:161], v[182:185], v[54:57]
	v_mfma_f32_16x16x32_bf16 v[46:49], v[166:169], v[182:185], v[46:49]
	v_mfma_f32_16x16x32_bf16 v[38:41], v[158:161], v[190:193], v[38:41]
	v_mfma_f32_16x16x32_bf16 v[30:33], v[166:169], v[190:193], v[30:33]
	v_mfma_f32_16x16x32_bf16 v[22:25], v[158:161], v[202:205], v[22:25]
	v_mfma_f32_16x16x32_bf16 v[14:17], v[166:169], v[202:205], v[14:17]
	s_barrier
	ds_read_b128 v[154:157], v150
	ds_read_b128 v[158:161], v150 offset:1024
	ds_read_b128 v[162:165], v150 offset:2048
	ds_read_b128 v[166:169], v150 offset:3072
	s_add_u32 s30, s30, 0x80080
	s_addc_u32 s31, s31, 0
	s_add_i32 s34, s34, s40
	v_lshl_add_u64 v[146:147], s[30:31], 0, v[132:133]
	s_mov_b32 m0, s34
	s_nop 0
	global_load_lds_dwordx4 v[146:147], off
	v_lshl_add_u64 v[146:147], s[30:31], 0, v[136:137]
	s_add_i32 m0, s34, 0x2000
	s_nop 0
	global_load_lds_dwordx4 v[146:147], off
	s_waitcnt vmcnt(6)
	s_barrier
	v_mfma_f32_16x16x32_bf16 v[50:53], v[206:209], v[170:173], v[50:53]
	v_mfma_f32_16x16x32_bf16 v[42:45], v[214:217], v[170:173], v[42:45]
	v_mfma_f32_16x16x32_bf16 v[34:37], v[206:209], v[178:181], v[34:37]
	v_mfma_f32_16x16x32_bf16 v[26:29], v[214:217], v[178:181], v[26:29]
	v_mfma_f32_16x16x32_bf16 v[18:21], v[206:209], v[186:189], v[18:21]
	v_mfma_f32_16x16x32_bf16 v[10:13], v[214:217], v[186:189], v[10:13]
	v_mfma_f32_16x16x32_bf16 v[6:9], v[206:209], v[198:201], v[6:9]
	v_mfma_f32_16x16x32_bf16 v[2:5], v[214:217], v[198:201], v[2:5]
	v_mfma_f32_16x16x32_bf16 v[50:53], v[210:213], v[174:177], v[50:53]
	v_mfma_f32_16x16x32_bf16 v[42:45], v[218:221], v[174:177], v[42:45]
	v_mfma_f32_16x16x32_bf16 v[34:37], v[210:213], v[182:185], v[34:37]
	v_mfma_f32_16x16x32_bf16 v[26:29], v[218:221], v[182:185], v[26:29]
	v_mfma_f32_16x16x32_bf16 v[18:21], v[210:213], v[190:193], v[18:21]
	v_mfma_f32_16x16x32_bf16 v[10:13], v[218:221], v[190:193], v[10:13]
	v_mfma_f32_16x16x32_bf16 v[6:9], v[210:213], v[202:205], v[6:9]
	v_mfma_f32_16x16x32_bf16 v[2:5], v[218:221], v[202:205], v[2:5]
	s_add_i32 s74, s74, 2
	s_add_u32 s28, s28, 0x100
	s_addc_u32 s29, s29, 0
	s_add_u32 s72, s72, 0x100
	s_addc_u32 s73, s73, 0
	s_cmp_gt_u32 s74, 29
	s_barrier
	s_cbranch_scc0 .LBB0_715
	s_waitcnt lgkmcnt(0)
	v_lshl_add_u32 v154, s26, 8, v1
	v_lshl_or_b32 v146, s69, 8, v149
	v_ashrrev_i32_e32 v155, 31, v154
	v_ashrrev_i32_e32 v147, 31, v146
	v_lshlrev_b64 v[156:157], 12, v[154:155]
	v_lshl_add_u64 v[156:157], s[6:7], 0, v[156:157]
	v_lshlrev_b64 v[158:159], 1, v[146:147]
	v_lshl_add_u64 v[146:147], v[156:157], 0, v[158:159]
	v_cvt_pk_bf16_f32 v126, v126, v127
	v_cvt_pk_bf16_f32 v127, v128, v129
	v_cvt_pk_bf16_f32 v128, v122, v123
	v_cvt_pk_bf16_f32 v129, v124, v125
	global_store_dwordx4 v[146:147], v[126:129], off
	v_cvt_pk_bf16_f32 v118, v118, v119
	v_cvt_pk_bf16_f32 v119, v120, v121
	v_cvt_pk_bf16_f32 v120, v110, v111
	v_or_b32_e32 v110, 16, v154
	v_ashrrev_i32_e32 v111, 31, v110
	v_lshlrev_b64 v[110:111], 12, v[110:111]
	v_lshl_add_u64 v[110:111], s[6:7], 0, v[110:111]
	v_cvt_pk_bf16_f32 v121, v112, v113
	global_store_dwordx4 v[146:147], v[118:121], off offset:256
	s_mov_b32 s69, s18
	s_mov_b32 s26, s20
	v_lshl_add_u64 v[118:119], v[110:111], 0, v[158:159]
	v_cvt_pk_bf16_f32 v110, v114, v115
	v_cvt_pk_bf16_f32 v111, v116, v117
	v_cvt_pk_bf16_f32 v112, v106, v107
	v_cvt_pk_bf16_f32 v113, v108, v109
	global_store_dwordx4 v[118:119], v[110:113], off
	v_cvt_pk_bf16_f32 v102, v102, v103
	v_cvt_pk_bf16_f32 v103, v104, v105
	v_cvt_pk_bf16_f32 v104, v94, v95
	v_or_b32_e32 v94, 32, v154
	v_ashrrev_i32_e32 v95, 31, v94
	v_lshlrev_b64 v[94:95], 12, v[94:95]
	v_lshl_add_u64 v[94:95], s[6:7], 0, v[94:95]
	v_cvt_pk_bf16_f32 v105, v96, v97
	global_store_dwordx4 v[118:119], v[102:105], off offset:256
	s_mov_b64 s[30:31], s[24:25]
	s_mov_b64 s[28:29], s[22:23]
	v_lshl_add_u64 v[102:103], v[94:95], 0, v[158:159]
	v_cvt_pk_bf16_f32 v94, v98, v99
	v_cvt_pk_bf16_f32 v95, v100, v101
	v_cvt_pk_bf16_f32 v96, v90, v91
	v_cvt_pk_bf16_f32 v97, v92, v93
	global_store_dwordx4 v[102:103], v[94:97], off
	v_cvt_pk_bf16_f32 v86, v86, v87
	v_cvt_pk_bf16_f32 v87, v88, v89
	v_cvt_pk_bf16_f32 v88, v78, v79
	v_or_b32_e32 v78, 48, v154
	v_ashrrev_i32_e32 v79, 31, v78
	v_lshlrev_b64 v[78:79], 12, v[78:79]
	v_lshl_add_u64 v[78:79], s[6:7], 0, v[78:79]
	v_cvt_pk_bf16_f32 v89, v80, v81
	global_store_dwordx4 v[102:103], v[86:89], off offset:256
	s_nop 1
	v_lshl_add_u64 v[86:87], v[78:79], 0, v[158:159]
	v_cvt_pk_bf16_f32 v78, v82, v83
	v_cvt_pk_bf16_f32 v79, v84, v85
	v_cvt_pk_bf16_f32 v80, v74, v75
	v_cvt_pk_bf16_f32 v81, v76, v77
	global_store_dwordx4 v[86:87], v[78:81], off
	v_cvt_pk_bf16_f32 v70, v70, v71
	v_cvt_pk_bf16_f32 v71, v72, v73
	v_cvt_pk_bf16_f32 v72, v66, v67
	v_cvt_pk_bf16_f32 v73, v68, v69
	global_store_dwordx4 v[86:87], v[70:73], off offset:256
	v_cvt_pk_bf16_f32 v62, v62, v63
	v_cvt_pk_bf16_f32 v63, v64, v65
	v_cvt_pk_bf16_f32 v64, v58, v59
	v_add_co_u32_e32 v58, vcc, s65, v146
	v_lshl_add_u64 v[66:67], v[146:147], 0, s[4:5]
	s_nop 0
	v_addc_co_u32_e32 v59, vcc, 0, v147, vcc
	v_cvt_pk_bf16_f32 v65, v60, v61
	global_store_dwordx4 v[58:59], v[62:65], off
	v_cvt_pk_bf16_f32 v50, v50, v51
	v_cvt_pk_bf16_f32 v51, v52, v53
	v_cvt_pk_bf16_f32 v52, v42, v43
	v_cvt_pk_bf16_f32 v53, v44, v45
	global_store_dwordx4 v[66:67], v[50:53], off offset:256
	v_cvt_pk_bf16_f32 v42, v54, v55
	v_cvt_pk_bf16_f32 v43, v56, v57
	v_cvt_pk_bf16_f32 v44, v46, v47
	v_add_co_u32_e32 v46, vcc, s66, v146
	s_nop 0
	v_lshl_add_u64 v[50:51], v[146:147], 0, s[10:11]
	v_addc_co_u32_e32 v47, vcc, 0, v147, vcc
	v_cvt_pk_bf16_f32 v45, v48, v49
	global_store_dwordx4 v[46:47], v[42:45], off
	v_cvt_pk_bf16_f32 v34, v34, v35
	v_cvt_pk_bf16_f32 v35, v36, v37
	v_cvt_pk_bf16_f32 v36, v26, v27
	v_cvt_pk_bf16_f32 v37, v28, v29
	global_store_dwordx4 v[50:51], v[34:37], off offset:256
	v_cvt_pk_bf16_f32 v26, v38, v39
	v_cvt_pk_bf16_f32 v27, v40, v41
	v_cvt_pk_bf16_f32 v28, v30, v31
	v_add_co_u32_e32 v30, vcc, s67, v146
	s_nop 0
	v_lshl_add_u64 v[34:35], v[146:147], 0, s[14:15]
	v_addc_co_u32_e32 v31, vcc, 0, v147, vcc
	v_cvt_pk_bf16_f32 v29, v32, v33
	global_store_dwordx4 v[30:31], v[26:29], off
	v_cvt_pk_bf16_f32 v18, v18, v19
	v_cvt_pk_bf16_f32 v19, v20, v21
	v_cvt_pk_bf16_f32 v20, v10, v11
	v_cvt_pk_bf16_f32 v21, v12, v13
	global_store_dwordx4 v[34:35], v[18:21], off offset:256
	v_cvt_pk_bf16_f32 v10, v22, v23
	v_cvt_pk_bf16_f32 v11, v24, v25
	v_cvt_pk_bf16_f32 v12, v14, v15
	v_add_co_u32_e32 v14, vcc, s68, v146
	s_nop 0
	v_lshl_add_u64 v[18:19], v[146:147], 0, s[16:17]
	v_addc_co_u32_e32 v15, vcc, 0, v147, vcc
	s_and_b64 vcc, exec, s[0:1]
	v_cvt_pk_bf16_f32 v13, v16, v17
	global_store_dwordx4 v[14:15], v[10:13], off
	v_cvt_pk_bf16_f32 v6, v6, v7
	v_cvt_pk_bf16_f32 v7, v8, v9
	v_cvt_pk_bf16_f32 v8, v2, v3
	v_cvt_pk_bf16_f32 v9, v4, v5
	global_store_dwordx4 v[18:19], v[6:9], off offset:256
	s_cbranch_vccz .LBB0_708
	s_waitcnt vmcnt(0)
	s_cmpk_gt_u32 s33, 0xff
	s_cbranch_scc1 .LBB0_719
	s_barrier

.LBB0_1060:
	s_add_u32 s4, s26, 0x100
	s_addc_u32 s5, s27, 0
	s_add_u32 s54, s50, s26
	s_addc_u32 s55, s51, s27
	s_cmp_eq_u32 s52, 12
	s_cselect_b64 vcc, -1, 0
	s_and_b64 s[24:25], vcc, exec
	s_cselect_b32 s53, 0, s4
	s_cselect_b32 s25, s21, s55
	s_cselect_b32 s24, s49, s54
	v_lshl_add_u64 v[18:19], v[186:187], 0, s[26:27]
	s_add_i32 m0, s33, 0xc000
	ds_read_b128 v[210:213], v203
	ds_read_b128 v[214:217], v203 offset:1024
	ds_read_b128 v[218:221], v203 offset:2048
	ds_read_b128 v[222:225], v203 offset:3072
	ds_read_b128 v[226:229], v203 offset:4096
	ds_read_b128 v[230:233], v203 offset:5120
	ds_read_b128 v[234:237], v203 offset:6144
	ds_read_b128 v[238:241], v203 offset:7168
	global_load_lds_dwordx4 v[18:19], off
	v_lshl_add_u64 v[18:19], v[184:185], 0, s[26:27]
	s_add_i32 m0, s33, 0xe000
	s_nop 0
	global_load_lds_dwordx4 v[18:19], off
	s_waitcnt lgkmcnt(8)
	s_barrier
	s_waitcnt lgkmcnt(0)
	s_waitcnt lgkmcnt(0)
	v_mfma_f32_16x16x128_f8f6f4 v[158:161], v[2:9], v[210:217], v[158:161]
	v_mfma_f32_16x16x128_f8f6f4 v[150:153], v[10:17], v[210:217], v[150:153]
	v_mfma_f32_16x16x128_f8f6f4 v[142:145], v[2:9], v[218:225], v[142:145]
	v_mfma_f32_16x16x128_f8f6f4 v[134:137], v[10:17], v[218:225], v[134:137]
	v_mfma_f32_16x16x128_f8f6f4 v[126:129], v[2:9], v[226:233], v[126:129]
	v_mfma_f32_16x16x128_f8f6f4 v[118:121], v[10:17], v[226:233], v[118:121]
	v_mfma_f32_16x16x128_f8f6f4 v[110:113], v[2:9], v[234:241], v[110:113]
	v_mfma_f32_16x16x128_f8f6f4 v[102:105], v[10:17], v[234:241], v[102:105]
	s_barrier
	s_add_i32 s26, s39, s23
	v_add_u32_e32 v30, s40, v201
	v_lshl_add_u64 v[188:189], s[24:25], 0, v[164:165]
	s_mov_b32 m0, s26
	ds_read_b128 v[18:21], v30
	ds_read_b128 v[22:25], v30 offset:1024
	ds_read_b128 v[26:29], v30 offset:2048
	ds_read_b128 v[30:33], v30 offset:3072
	global_load_lds_dwordx4 v[188:189], off
	v_lshl_add_u64 v[190:191], s[24:25], 0, v[166:167]
	s_add_i32 m0, s26, 0x2000
	s_nop 0
	global_load_lds_dwordx4 v[190:191], off
	s_barrier
	s_waitcnt lgkmcnt(0)
	s_waitcnt lgkmcnt(0)
	v_mfma_f32_16x16x128_f8f6f4 v[154:157], v[18:25], v[210:217], v[154:157]
	v_mfma_f32_16x16x128_f8f6f4 v[146:149], v[26:33], v[210:217], v[146:149]
	v_mfma_f32_16x16x128_f8f6f4 v[138:141], v[18:25], v[218:225], v[138:141]
	v_mfma_f32_16x16x128_f8f6f4 v[130:133], v[26:33], v[218:225], v[130:133]
	v_mfma_f32_16x16x128_f8f6f4 v[122:125], v[18:25], v[226:233], v[122:125]
	v_mfma_f32_16x16x128_f8f6f4 v[114:117], v[26:33], v[226:233], v[114:117]
	v_mfma_f32_16x16x128_f8f6f4 v[106:109], v[18:25], v[234:241], v[106:109]
	v_mfma_f32_16x16x128_f8f6f4 v[98:101], v[26:33], v[234:241], v[98:101]
	s_add_u32 s26, s10, s53
	s_mov_b32 m0, s33
	s_addc_u32 s27, s11, 0
	v_cndmask_b32_e32 v162, v208, v206, vcc
	s_barrier
	ds_read_b128 v[210:213], v203 offset:16384
	ds_read_b128 v[214:217], v203 offset:17408
	ds_read_b128 v[218:221], v203 offset:18432
	ds_read_b128 v[222:225], v203 offset:19456
	ds_read_b128 v[226:229], v203 offset:20480
	ds_read_b128 v[230:233], v203 offset:21504
	ds_read_b128 v[234:237], v203 offset:22528
	ds_read_b128 v[238:241], v203 offset:23552
	v_cndmask_b32_e32 v192, v178, v207, vcc
	global_load_lds_dwordx4 v162, s[26:27]
	s_mov_b32 m0, s34
	v_mov_b32_e32 v193, v163
	global_load_lds_dwordx4 v192, s[26:27]
	s_waitcnt vmcnt(10)
	s_barrier
	s_waitcnt lgkmcnt(0)
	v_lshl_add_u64 v[194:195], s[26:27], 0, v[162:163]
	v_lshl_add_u64 v[192:193], s[26:27], 0, v[192:193]
	s_waitcnt lgkmcnt(0)
	v_mfma_f32_16x16x128_f8f6f4 v[94:97], v[2:9], v[210:217], v[94:97]
	v_mfma_f32_16x16x128_f8f6f4 v[86:89], v[10:17], v[210:217], v[86:89]
	v_mfma_f32_16x16x128_f8f6f4 v[78:81], v[2:9], v[218:225], v[78:81]
	v_mfma_f32_16x16x128_f8f6f4 v[70:73], v[10:17], v[218:225], v[70:73]
	v_mfma_f32_16x16x128_f8f6f4 v[62:65], v[2:9], v[226:233], v[62:65]
	v_mfma_f32_16x16x128_f8f6f4 v[54:57], v[10:17], v[226:233], v[54:57]
	v_mfma_f32_16x16x128_f8f6f4 v[46:49], v[2:9], v[234:241], v[46:49]
	v_mfma_f32_16x16x128_f8f6f4 v[38:41], v[10:17], v[234:241], v[38:41]
	s_barrier
	v_add_u32_e32 v14, 0x18000, v201
	ds_read_b128 v[2:5], v14
	ds_read_b128 v[6:9], v14 offset:1024
	ds_read_b128 v[10:13], v14 offset:2048
	ds_read_b128 v[14:17], v14 offset:3072
	s_add_u32 s54, s24, 0x40000
	s_addc_u32 s55, s25, 0
	s_add_i32 s53, s40, s23
	v_lshl_add_u64 v[242:243], s[54:55], 0, v[164:165]
	s_mov_b32 m0, s53
	s_nop 0
	global_load_lds_dwordx4 v[242:243], off
	v_lshl_add_u64 v[242:243], s[54:55], 0, v[166:167]
	s_add_i32 m0, s53, 0x2000
	s_nop 0
	global_load_lds_dwordx4 v[242:243], off
	s_waitcnt vmcnt(6)
	s_barrier
	v_mfma_f32_16x16x128_f8f6f4 v[90:93], v[18:25], v[210:217], v[90:93]
	v_mfma_f32_16x16x128_f8f6f4 v[82:85], v[26:33], v[210:217], v[82:85]
	v_mfma_f32_16x16x128_f8f6f4 v[74:77], v[18:25], v[218:225], v[74:77]
	v_mfma_f32_16x16x128_f8f6f4 v[66:69], v[26:33], v[218:225], v[66:69]
	v_mfma_f32_16x16x128_f8f6f4 v[58:61], v[18:25], v[226:233], v[58:61]
	v_mfma_f32_16x16x128_f8f6f4 v[50:53], v[26:33], v[226:233], v[50:53]
	v_mfma_f32_16x16x128_f8f6f4 v[42:45], v[18:25], v[234:241], v[42:45]
	v_mfma_f32_16x16x128_f8f6f4 v[34:37], v[26:33], v[234:241], v[34:37]
	s_add_i32 s53, 0, 0x18000
	s_barrier
	v_cndmask_b32_e32 v172, v180, v174, vcc
	s_mov_b32 m0, s35
	v_cndmask_b32_e32 v226, v182, v176, vcc
	v_mov_b32_e32 v227, v173
	v_lshl_add_u64 v[228:229], s[26:27], 0, v[172:173]
	ds_read_b128 v[18:21], v203 offset:32768
	ds_read_b128 v[22:25], v203 offset:33792
	ds_read_b128 v[26:29], v203 offset:34816
	ds_read_b128 v[30:33], v203 offset:35840
	ds_read_b128 v[210:213], v203 offset:36864
	ds_read_b128 v[214:217], v203 offset:37888
	ds_read_b128 v[218:221], v203 offset:38912
	ds_read_b128 v[222:225], v203 offset:39936
	global_load_lds_dwordx4 v[228:229], off
	v_lshl_add_u64 v[226:227], s[26:27], 0, v[226:227]
	s_mov_b32 m0, s36
	s_nop 0
	global_load_lds_dwordx4 v[226:227], off
	s_waitcnt lgkmcnt(8)
	s_barrier
	s_waitcnt lgkmcnt(0)
	s_waitcnt lgkmcnt(0)
	v_mfma_f32_16x16x128_f8f6f4 v[158:161], v[2:9], v[18:25], v[158:161]
	v_mfma_f32_16x16x128_f8f6f4 v[150:153], v[10:17], v[18:25], v[150:153]
	v_mfma_f32_16x16x128_f8f6f4 v[142:145], v[2:9], v[26:33], v[142:145]
	v_mfma_f32_16x16x128_f8f6f4 v[134:137], v[10:17], v[26:33], v[134:137]
	v_mfma_f32_16x16x128_f8f6f4 v[126:129], v[2:9], v[210:217], v[126:129]
	v_mfma_f32_16x16x128_f8f6f4 v[118:121], v[10:17], v[210:217], v[118:121]
	v_mfma_f32_16x16x128_f8f6f4 v[110:113], v[2:9], v[218:225], v[110:113]
	v_mfma_f32_16x16x128_f8f6f4 v[102:105], v[10:17], v[218:225], v[102:105]
	s_barrier
	s_add_i32 s26, 0, 0x1c000
	s_add_i32 s27, s53, s23
	v_add_u32_e32 v162, s26, v201
	s_add_i32 m0, s27, 0xffffff80
	ds_read_b128 v[226:229], v162
	ds_read_b128 v[230:233], v162 offset:1024
	ds_read_b128 v[234:237], v162 offset:2048
	ds_read_b128 v[238:241], v162 offset:3072
	global_load_lds_dwordx4 v[188:189], off offset:128
	s_add_i32 m0, s27, 0x1f80
	s_nop 0
	global_load_lds_dwordx4 v[190:191], off offset:128
	s_barrier
	s_waitcnt lgkmcnt(0)
	s_waitcnt lgkmcnt(0)
	v_mfma_f32_16x16x128_f8f6f4 v[154:157], v[226:233], v[18:25], v[154:157]
	v_mfma_f32_16x16x128_f8f6f4 v[146:149], v[234:241], v[18:25], v[146:149]
	v_mfma_f32_16x16x128_f8f6f4 v[138:141], v[226:233], v[26:33], v[138:141]
	v_mfma_f32_16x16x128_f8f6f4 v[130:133], v[234:241], v[26:33], v[130:133]
	v_mfma_f32_16x16x128_f8f6f4 v[122:125], v[226:233], v[210:217], v[122:125]
	v_mfma_f32_16x16x128_f8f6f4 v[114:117], v[234:241], v[210:217], v[114:117]
	v_mfma_f32_16x16x128_f8f6f4 v[106:109], v[226:233], v[218:225], v[106:109]
	v_mfma_f32_16x16x128_f8f6f4 v[98:101], v[234:241], v[218:225], v[98:101]
	s_add_i32 m0, s37, 0xffffff80
	s_barrier
	ds_read_b128 v[18:21], v203 offset:49152
	ds_read_b128 v[22:25], v203 offset:50176
	ds_read_b128 v[26:29], v203 offset:51200
	ds_read_b128 v[30:33], v203 offset:52224
	ds_read_b128 v[210:213], v203 offset:53248
	ds_read_b128 v[214:217], v203 offset:54272
	ds_read_b128 v[218:221], v203 offset:55296
	ds_read_b128 v[222:225], v203 offset:56320
	global_load_lds_dwordx4 v[194:195], off offset:128
	s_add_i32 m0, s38, 0xffffff80
	s_nop 0
	global_load_lds_dwordx4 v[192:193], off offset:128
	s_waitcnt vmcnt(10)
	s_barrier
	s_waitcnt lgkmcnt(0)
	s_waitcnt lgkmcnt(0)
	v_mfma_f32_16x16x128_f8f6f4 v[94:97], v[2:9], v[18:25], v[94:97]
	v_mfma_f32_16x16x128_f8f6f4 v[86:89], v[10:17], v[18:25], v[86:89]
	v_mfma_f32_16x16x128_f8f6f4 v[78:81], v[2:9], v[26:33], v[78:81]
	v_mfma_f32_16x16x128_f8f6f4 v[70:73], v[10:17], v[26:33], v[70:73]
	v_mfma_f32_16x16x128_f8f6f4 v[62:65], v[2:9], v[210:217], v[62:65]
	v_mfma_f32_16x16x128_f8f6f4 v[54:57], v[10:17], v[210:217], v[54:57]
	v_mfma_f32_16x16x128_f8f6f4 v[46:49], v[2:9], v[218:225], v[46:49]
	v_mfma_f32_16x16x128_f8f6f4 v[38:41], v[10:17], v[218:225], v[38:41]
	s_barrier
	v_add_u32_e32 v14, s39, v201
	ds_read_b128 v[2:5], v14
	ds_read_b128 v[6:9], v14 offset:1024
	ds_read_b128 v[10:13], v14 offset:2048
	ds_read_b128 v[14:17], v14 offset:3072
	s_add_u32 s24, s24, 0x40080
	s_addc_u32 s25, s25, 0
	s_add_i32 s26, s26, s23
	v_lshl_add_u64 v[242:243], s[24:25], 0, v[164:165]
	s_mov_b32 m0, s26
	s_nop 0
	global_load_lds_dwordx4 v[242:243], off
	v_lshl_add_u64 v[242:243], s[24:25], 0, v[166:167]
	s_add_i32 m0, s26, 0x2000
	s_nop 0
	global_load_lds_dwordx4 v[242:243], off
	s_waitcnt vmcnt(6)
	s_barrier
	v_mfma_f32_16x16x128_f8f6f4 v[90:93], v[226:233], v[18:25], v[90:93]
	v_mfma_f32_16x16x128_f8f6f4 v[82:85], v[234:241], v[18:25], v[82:85]
	v_mfma_f32_16x16x128_f8f6f4 v[74:77], v[226:233], v[26:33], v[74:77]
	v_mfma_f32_16x16x128_f8f6f4 v[66:69], v[234:241], v[26:33], v[66:69]
	v_mfma_f32_16x16x128_f8f6f4 v[58:61], v[226:233], v[210:217], v[58:61]
	v_mfma_f32_16x16x128_f8f6f4 v[50:53], v[234:241], v[210:217], v[50:53]
	v_mfma_f32_16x16x128_f8f6f4 v[42:45], v[226:233], v[218:225], v[42:45]
	v_mfma_f32_16x16x128_f8f6f4 v[34:37], v[234:241], v[218:225], v[34:37]
	s_add_i32 s52, s52, 2
	s_cmp_gt_u32 s52, 13
	s_mov_b64 s[26:27], s[4:5]
	s_barrier
	s_cbranch_scc0 .LBB0_1060
	s_waitcnt lgkmcnt(0)
	v_mov_b32_e32 v2, v158
	v_mov_b32_e32 v3, v154
	v_pk_mul_f32 v[2:3], v[2:3], s[18:19] op_sel_hi:[1,0]
	v_mov_b32_e32 v154, v159
	v_mul_f32_e32 v5, 0xbfb8aa3b, v2
	v_pk_mul_f32 v[6:7], v[154:155], s[18:19] op_sel_hi:[1,0]
	v_exp_f32_e32 v8, v5
	v_mul_f32_e32 v5, 0xbfb8aa3b, v6
	v_exp_f32_e32 v9, v5
	v_mul_f32_e32 v2, v2, v3
	v_add_f32_e32 v8, 1.0, v8
	v_rcp_f32_e32 v8, v8
	v_add_f32_e32 v9, 1.0, v9
	v_rcp_f32_e32 v9, v9
	v_mov_b32_e32 v3, v156
	v_mul_f32_e32 v8, v8, v2
	v_mul_f32_e32 v2, v6, v7
	v_mul_f32_e32 v9, v9, v2
	v_mov_b32_e32 v2, v160
	v_pk_mul_f32 v[2:3], v[2:3], s[18:19] op_sel_hi:[1,0]
	v_mov_b32_e32 v156, v161
	v_mul_f32_e32 v6, 0xbfb8aa3b, v2
	v_exp_f32_e32 v10, v6
	v_pk_mul_f32 v[6:7], v[156:157], s[18:19] op_sel_hi:[1,0]
	v_mul_f32_e32 v12, v2, v3
	v_mul_f32_e32 v11, 0xbfb8aa3b, v6
	v_exp_f32_e32 v11, v11
	v_add_f32_e32 v2, 1.0, v10
	v_rcp_f32_e32 v10, v2
	v_mov_b32_e32 v3, v146
	v_add_f32_e32 v2, 1.0, v11
	v_rcp_f32_e32 v11, v2
	v_mov_b32_e32 v2, v150
	v_pk_mul_f32 v[2:3], v[2:3], s[18:19] op_sel_hi:[1,0]
	v_mul_f32_e32 v6, v6, v7
	v_mul_f32_e32 v13, 0xbfb8aa3b, v2
	v_exp_f32_e32 v13, v13
	v_mul_f32_e32 v11, v11, v6
	v_mov_b32_e32 v146, v151
	v_mul_f32_e32 v10, v10, v12
	v_add_f32_e32 v6, 1.0, v13
	v_rcp_f32_e32 v12, v6
	v_pk_mul_f32 v[6:7], v[146:147], s[18:19] op_sel_hi:[1,0]
	v_mul_f32_e32 v2, v2, v3
	v_mul_f32_e32 v13, 0xbfb8aa3b, v6
	v_exp_f32_e32 v13, v13
	v_mul_f32_e32 v12, v12, v2
	v_mov_b32_e32 v3, v148
	v_mul_f32_e32 v14, v6, v7
	v_add_f32_e32 v2, 1.0, v13
	v_rcp_f32_e32 v13, v2
	v_mov_b32_e32 v2, v152
	v_pk_mul_f32 v[2:3], v[2:3], s[18:19] op_sel_hi:[1,0]
	v_mov_b32_e32 v148, v153
	v_mul_f32_e32 v6, 0xbfb8aa3b, v2
	v_exp_f32_e32 v15, v6
	v_pk_mul_f32 v[6:7], v[148:149], s[18:19] op_sel_hi:[1,0]
	v_mul_f32_e32 v13, v13, v14
	v_mul_f32_e32 v16, 0xbfb8aa3b, v6
	v_exp_f32_e32 v16, v16
	v_add_f32_e32 v14, 1.0, v15
	v_rcp_f32_e32 v14, v14
	v_mul_f32_e32 v2, v2, v3
	v_add_f32_e32 v15, 1.0, v16
	v_rcp_f32_e32 v15, v15
	v_mul_f32_e32 v3, v6, v7
	v_mul_f32_e32 v6, 4.0, v8
	v_mul_f32_e32 v7, 4.0, v9
	v_mul_f32_e32 v8, 4.0, v10
	v_mul_f32_e32 v9, 4.0, v11
	v_mul_f32_e32 v10, 4.0, v12
	v_mul_f32_e32 v11, 4.0, v13
	v_med3_f32 v12, v6, s41, v205
	v_med3_f32 v7, v7, s41, v205
	v_mov_b32_e32 v6, v163
	v_cvt_pk_fp8_f32 v6, v12, v7
	v_med3_f32 v10, v10, s41, v205
	v_med3_f32 v11, v11, s41, v205
	v_mov_b32_e32 v7, v163
	v_cvt_pk_fp8_f32 v7, v10, v11
	v_mul_f32_e32 v2, v14, v2
	v_mul_f32_e32 v3, v15, v3
	v_mul_f32_e32 v2, 4.0, v2
	v_mul_f32_e32 v3, 4.0, v3
	v_lshl_add_u32 v4, s48, 8, v179
	v_med3_f32 v8, v8, s41, v205
	v_med3_f32 v9, v9, s41, v205
	v_med3_f32 v2, v2, s41, v205
	v_med3_f32 v3, v3, s41, v205
	s_lshl_b32 s4, s22, 7
	v_ashrrev_i32_e32 v5, 31, v4
	v_cvt_pk_fp8_f32 v6, v8, v9 op_sel:[0,0,1]
	v_cvt_pk_fp8_f32 v7, v2, v3 op_sel:[0,0,1]
	s_and_b32 s4, s4, 0x780
	v_lshlrev_b64 v[2:3], 11, v[4:5]
	v_mov_b32_e32 v8, v142
	v_mov_b32_e32 v9, v138
	v_or_b32_e32 v162, s4, v202
	v_lshl_add_u64 v[2:3], s[12:13], 0, v[2:3]
	v_pk_mul_f32 v[8:9], v[8:9], s[18:19] op_sel_hi:[1,0]
	v_mov_b32_e32 v138, v143
	v_lshl_add_u64 v[2:3], v[2:3], 0, v[162:163]
	v_mul_f32_e32 v5, 0xbfb8aa3b, v8
	v_pk_mul_f32 v[10:11], v[138:139], s[18:19] op_sel_hi:[1,0]
	s_nop 15
	s_nop 15
	global_store_dwordx2 v[2:3], v[6:7], off
	v_exp_f32_e32 v5, v5
	v_mul_f32_e32 v7, 0xbfb8aa3b, v10
	v_exp_f32_e32 v12, v7
	v_mul_f32_e32 v8, v8, v9
	v_add_f32_e32 v5, 1.0, v5
	v_rcp_f32_e32 v5, v5
	v_add_f32_e32 v12, 1.0, v12
	v_rcp_f32_e32 v12, v12
	v_mov_b32_e32 v9, v140
	v_mul_f32_e32 v5, v5, v8
	v_mul_f32_e32 v8, v10, v11
	v_mul_f32_e32 v12, v12, v8
	v_mov_b32_e32 v8, v144
	v_pk_mul_f32 v[8:9], v[8:9], s[18:19] op_sel_hi:[1,0]
	v_mov_b32_e32 v140, v145
	v_mul_f32_e32 v10, 0xbfb8aa3b, v8
	v_exp_f32_e32 v13, v10
	v_pk_mul_f32 v[10:11], v[140:141], s[18:19] op_sel_hi:[1,0]
	v_mul_f32_e32 v15, v8, v9
	v_mul_f32_e32 v14, 0xbfb8aa3b, v10
	v_exp_f32_e32 v14, v14
	v_add_f32_e32 v8, 1.0, v13
	v_rcp_f32_e32 v13, v8
	v_mov_b32_e32 v9, v130
	v_add_f32_e32 v8, 1.0, v14
	v_rcp_f32_e32 v14, v8
	v_mov_b32_e32 v8, v134
	v_pk_mul_f32 v[8:9], v[8:9], s[18:19] op_sel_hi:[1,0]
	v_mul_f32_e32 v10, v10, v11
	v_mul_f32_e32 v16, 0xbfb8aa3b, v8
	v_exp_f32_e32 v16, v16
	v_mul_f32_e32 v14, v14, v10
	v_mov_b32_e32 v130, v135
	v_mul_f32_e32 v13, v13, v15
	v_add_f32_e32 v10, 1.0, v16
	v_rcp_f32_e32 v15, v10
	v_pk_mul_f32 v[10:11], v[130:131], s[18:19] op_sel_hi:[1,0]
	v_mul_f32_e32 v8, v8, v9
	v_mul_f32_e32 v16, 0xbfb8aa3b, v10
	v_exp_f32_e32 v16, v16
	v_mul_f32_e32 v15, v15, v8
	v_mov_b32_e32 v9, v132
	v_mul_f32_e32 v17, v10, v11
	v_add_f32_e32 v8, 1.0, v16
	v_rcp_f32_e32 v16, v8
	v_mov_b32_e32 v8, v136
	v_pk_mul_f32 v[8:9], v[8:9], s[18:19] op_sel_hi:[1,0]
	v_mov_b32_e32 v132, v137
	v_mul_f32_e32 v10, 0xbfb8aa3b, v8
	v_exp_f32_e32 v18, v10
	v_pk_mul_f32 v[10:11], v[132:133], s[18:19] op_sel_hi:[1,0]
	v_mul_f32_e32 v16, v16, v17
	v_mul_f32_e32 v19, 0xbfb8aa3b, v10
	v_exp_f32_e32 v19, v19
	v_add_f32_e32 v17, 1.0, v18
	v_rcp_f32_e32 v17, v17
	v_mul_f32_e32 v8, v8, v9
	v_add_f32_e32 v18, 1.0, v19
	v_rcp_f32_e32 v18, v18
	v_mul_f32_e32 v9, v10, v11
	v_mul_f32_e32 v8, v17, v8
	v_mul_f32_e32 v5, 4.0, v5
	v_mul_f32_e32 v9, v18, v9
	v_mul_f32_e32 v10, 4.0, v12
	v_mul_f32_e32 v11, 4.0, v13
	v_mul_f32_e32 v12, 4.0, v14
	v_mul_f32_e32 v13, 4.0, v15
	v_mul_f32_e32 v14, 4.0, v16
	v_mul_f32_e32 v15, 4.0, v8
	v_mul_f32_e32 v16, 4.0, v9
	v_med3_f32 v5, v5, s41, v205
	v_med3_f32 v9, v10, s41, v205
	v_mov_b32_e32 v8, v163
	v_cvt_pk_fp8_f32 v8, v5, v9
	v_med3_f32 v5, v11, s41, v205
	v_med3_f32 v10, v12, s41, v205
	v_med3_f32 v11, v13, s41, v205
	v_med3_f32 v12, v14, s41, v205
	v_mov_b32_e32 v9, v163
	v_cvt_pk_fp8_f32 v9, v11, v12
	v_or_b32_e32 v6, 16, v4
	v_cvt_pk_fp8_f32 v8, v5, v10 op_sel:[0,0,1]
	v_med3_f32 v5, v15, s41, v205
	v_med3_f32 v10, v16, s41, v205
	v_ashrrev_i32_e32 v7, 31, v6
	v_cvt_pk_fp8_f32 v9, v5, v10 op_sel:[0,0,1]
	v_lshlrev_b64 v[6:7], 11, v[6:7]
	v_lshl_add_u64 v[6:7], s[12:13], 0, v[6:7]
	v_lshl_add_u64 v[6:7], v[6:7], 0, v[162:163]
	global_store_dwordx2 v[6:7], v[8:9], off
	v_mov_b32_e32 v8, v126
	v_mov_b32_e32 v9, v122
	v_pk_mul_f32 v[8:9], v[8:9], s[18:19] op_sel_hi:[1,0]
	v_mov_b32_e32 v122, v127
	v_mul_f32_e32 v5, 0xbfb8aa3b, v8
	v_pk_mul_f32 v[10:11], v[122:123], s[18:19] op_sel_hi:[1,0]
	v_exp_f32_e32 v5, v5
	v_mul_f32_e32 v7, 0xbfb8aa3b, v10
	v_exp_f32_e32 v12, v7
	v_mul_f32_e32 v8, v8, v9
	v_add_f32_e32 v5, 1.0, v5
	v_rcp_f32_e32 v5, v5
	v_add_f32_e32 v12, 1.0, v12
	v_rcp_f32_e32 v12, v12
	v_mov_b32_e32 v9, v124
	v_mul_f32_e32 v5, v5, v8
	v_mul_f32_e32 v8, v10, v11
	v_mul_f32_e32 v12, v12, v8
	v_mov_b32_e32 v8, v128
	v_pk_mul_f32 v[8:9], v[8:9], s[18:19] op_sel_hi:[1,0]
	v_mov_b32_e32 v124, v129
	v_mul_f32_e32 v10, 0xbfb8aa3b, v8
	v_exp_f32_e32 v13, v10
	v_pk_mul_f32 v[10:11], v[124:125], s[18:19] op_sel_hi:[1,0]
	v_mul_f32_e32 v15, v8, v9
	v_mul_f32_e32 v14, 0xbfb8aa3b, v10
	v_exp_f32_e32 v14, v14
	v_add_f32_e32 v8, 1.0, v13
	v_rcp_f32_e32 v13, v8
	v_mov_b32_e32 v9, v114
	v_add_f32_e32 v8, 1.0, v14
	v_rcp_f32_e32 v14, v8
	v_mov_b32_e32 v8, v118
	v_pk_mul_f32 v[8:9], v[8:9], s[18:19] op_sel_hi:[1,0]
	v_mul_f32_e32 v10, v10, v11
	v_mul_f32_e32 v16, 0xbfb8aa3b, v8
	v_exp_f32_e32 v16, v16
	v_mul_f32_e32 v14, v14, v10
	v_mov_b32_e32 v114, v119
	v_mul_f32_e32 v13, v13, v15
	v_add_f32_e32 v10, 1.0, v16
	v_rcp_f32_e32 v15, v10
	v_pk_mul_f32 v[10:11], v[114:115], s[18:19] op_sel_hi:[1,0]
	v_mul_f32_e32 v8, v8, v9
	v_mul_f32_e32 v16, 0xbfb8aa3b, v10
	v_exp_f32_e32 v16, v16
	v_mul_f32_e32 v15, v15, v8
	v_mov_b32_e32 v9, v116
	v_mul_f32_e32 v17, v10, v11
	v_add_f32_e32 v8, 1.0, v16
	v_rcp_f32_e32 v16, v8
	v_mov_b32_e32 v8, v120
	v_pk_mul_f32 v[8:9], v[8:9], s[18:19] op_sel_hi:[1,0]
	v_mov_b32_e32 v116, v121
	v_mul_f32_e32 v10, 0xbfb8aa3b, v8
	v_exp_f32_e32 v18, v10
	v_pk_mul_f32 v[10:11], v[116:117], s[18:19] op_sel_hi:[1,0]
	v_mul_f32_e32 v16, v16, v17
	v_mul_f32_e32 v19, 0xbfb8aa3b, v10
	v_exp_f32_e32 v19, v19
	v_add_f32_e32 v17, 1.0, v18
	v_rcp_f32_e32 v17, v17
	v_mul_f32_e32 v8, v8, v9
	v_add_f32_e32 v18, 1.0, v19
	v_rcp_f32_e32 v18, v18
	v_mul_f32_e32 v9, v10, v11
	v_mul_f32_e32 v8, v17, v8
	v_mul_f32_e32 v5, 4.0, v5
	v_mul_f32_e32 v9, v18, v9
	v_mul_f32_e32 v10, 4.0, v12
	v_mul_f32_e32 v11, 4.0, v13
	v_mul_f32_e32 v12, 4.0, v14
	v_mul_f32_e32 v13, 4.0, v15
	v_mul_f32_e32 v14, 4.0, v16
	v_mul_f32_e32 v15, 4.0, v8
	v_mul_f32_e32 v16, 4.0, v9
	v_med3_f32 v5, v5, s41, v205
	v_med3_f32 v9, v10, s41, v205
	v_mov_b32_e32 v8, v163
	v_cvt_pk_fp8_f32 v8, v5, v9
	v_med3_f32 v5, v11, s41, v205
	v_med3_f32 v10, v12, s41, v205
	v_med3_f32 v11, v13, s41, v205
	v_med3_f32 v12, v14, s41, v205
	v_mov_b32_e32 v9, v163
	v_cvt_pk_fp8_f32 v9, v11, v12
	v_or_b32_e32 v6, 32, v4
	v_cvt_pk_fp8_f32 v8, v5, v10 op_sel:[0,0,1]
	v_med3_f32 v5, v15, s41, v205
	v_med3_f32 v10, v16, s41, v205
	v_ashrrev_i32_e32 v7, 31, v6
	v_cvt_pk_fp8_f32 v9, v5, v10 op_sel:[0,0,1]
	v_lshlrev_b64 v[6:7], 11, v[6:7]
	v_lshl_add_u64 v[6:7], s[12:13], 0, v[6:7]
	v_lshl_add_u64 v[6:7], v[6:7], 0, v[162:163]
	global_store_dwordx2 v[6:7], v[8:9], off
	v_mov_b32_e32 v6, v110
	v_mov_b32_e32 v7, v106
	v_pk_mul_f32 v[6:7], v[6:7], s[18:19] op_sel_hi:[1,0]
	v_mov_b32_e32 v106, v111
	v_mul_f32_e32 v8, 0xbfb8aa3b, v6
	v_exp_f32_e32 v10, v8
	v_pk_mul_f32 v[8:9], v[106:107], s[18:19] op_sel_hi:[1,0]
	v_mul_f32_e32 v6, v6, v7
	v_mul_f32_e32 v11, 0xbfb8aa3b, v8
	v_exp_f32_e32 v11, v11
	v_add_f32_e32 v10, 1.0, v10
	v_rcp_f32_e32 v10, v10
	v_mov_b32_e32 v7, v108
	v_add_f32_e32 v11, 1.0, v11
	v_rcp_f32_e32 v11, v11
	v_mul_f32_e32 v10, v10, v6
	v_mul_f32_e32 v6, v8, v9
	v_mov_b32_e32 v108, v113
	v_mul_f32_e32 v11, v11, v6
	v_mov_b32_e32 v6, v112
	v_pk_mul_f32 v[6:7], v[6:7], s[18:19] op_sel_hi:[1,0]
	v_or_b32_e32 v4, 48, v4
	v_mul_f32_e32 v8, 0xbfb8aa3b, v6
	v_exp_f32_e32 v12, v8
	v_pk_mul_f32 v[8:9], v[108:109], s[18:19] op_sel_hi:[1,0]
	v_mul_f32_e32 v14, v6, v7
	v_mul_f32_e32 v13, 0xbfb8aa3b, v8
	v_exp_f32_e32 v13, v13
	v_add_f32_e32 v6, 1.0, v12
	v_rcp_f32_e32 v12, v6
	v_mov_b32_e32 v7, v98
	v_add_f32_e32 v6, 1.0, v13
	v_rcp_f32_e32 v13, v6
	v_mov_b32_e32 v6, v102
	v_pk_mul_f32 v[6:7], v[6:7], s[18:19] op_sel_hi:[1,0]
	v_mul_f32_e32 v8, v8, v9
	v_mul_f32_e32 v15, 0xbfb8aa3b, v6
	v_exp_f32_e32 v15, v15
	v_mul_f32_e32 v13, v13, v8
	v_mov_b32_e32 v98, v103
	v_mul_f32_e32 v12, v12, v14
	v_add_f32_e32 v8, 1.0, v15
	v_rcp_f32_e32 v14, v8
	v_pk_mul_f32 v[8:9], v[98:99], s[18:19] op_sel_hi:[1,0]
	v_mul_f32_e32 v6, v6, v7
	v_mul_f32_e32 v15, 0xbfb8aa3b, v8
	v_exp_f32_e32 v15, v15
	v_mul_f32_e32 v14, v14, v6
	v_mov_b32_e32 v7, v100
	v_mul_f32_e32 v16, v8, v9
	v_add_f32_e32 v6, 1.0, v15
	v_rcp_f32_e32 v15, v6
	v_mov_b32_e32 v6, v104
	v_pk_mul_f32 v[6:7], v[6:7], s[18:19] op_sel_hi:[1,0]
	v_mov_b32_e32 v100, v105
	v_mul_f32_e32 v8, 0xbfb8aa3b, v6
	v_exp_f32_e32 v17, v8
	v_pk_mul_f32 v[8:9], v[100:101], s[18:19] op_sel_hi:[1,0]
	v_mul_f32_e32 v15, v15, v16
	v_mul_f32_e32 v18, 0xbfb8aa3b, v8
	v_exp_f32_e32 v18, v18
	v_add_f32_e32 v16, 1.0, v17
	v_rcp_f32_e32 v16, v16
	v_mul_f32_e32 v6, v6, v7
	v_add_f32_e32 v17, 1.0, v18
	v_rcp_f32_e32 v17, v17
	v_mul_f32_e32 v7, v8, v9
	v_mul_f32_e32 v6, v16, v6
	v_mul_f32_e32 v8, 4.0, v10
	v_mul_f32_e32 v7, v17, v7
	v_mul_f32_e32 v9, 4.0, v11
	v_mul_f32_e32 v10, 4.0, v12
	v_mul_f32_e32 v11, 4.0, v13
	v_mul_f32_e32 v12, 4.0, v14
	v_mul_f32_e32 v13, 4.0, v15
	v_mul_f32_e32 v14, 4.0, v6
	v_mul_f32_e32 v15, 4.0, v7
	v_med3_f32 v7, v8, s41, v205
	v_med3_f32 v8, v9, s41, v205
	v_mov_b32_e32 v6, v163
	v_cvt_pk_fp8_f32 v6, v7, v8
	v_med3_f32 v8, v10, s41, v205
	v_med3_f32 v9, v11, s41, v205
	v_med3_f32 v10, v12, s41, v205
	v_med3_f32 v11, v13, s41, v205
	v_mov_b32_e32 v7, v163
	v_cvt_pk_fp8_f32 v7, v10, v11
	v_cvt_pk_fp8_f32 v6, v8, v9 op_sel:[0,0,1]
	v_med3_f32 v8, v14, s41, v205
	v_med3_f32 v9, v15, s41, v205
	v_cvt_pk_fp8_f32 v7, v8, v9 op_sel:[0,0,1]
	v_mov_b32_e32 v8, v94
	v_mov_b32_e32 v9, v90
	v_pk_mul_f32 v[8:9], v[8:9], s[18:19] op_sel_hi:[1,0]
	v_mov_b32_e32 v90, v95
	v_mul_f32_e32 v10, 0xbfb8aa3b, v8
	v_exp_f32_e32 v12, v10
	v_pk_mul_f32 v[10:11], v[90:91], s[18:19] op_sel_hi:[1,0]
	v_ashrrev_i32_e32 v5, 31, v4
	v_mul_f32_e32 v13, 0xbfb8aa3b, v10
	v_lshlrev_b64 v[4:5], 11, v[4:5]
	v_exp_f32_e32 v13, v13
	v_lshl_add_u64 v[4:5], s[12:13], 0, v[4:5]
	v_lshl_add_u64 v[4:5], v[4:5], 0, v[162:163]
	global_store_dwordx2 v[4:5], v[6:7], off
	v_add_f32_e32 v4, 1.0, v12
	v_rcp_f32_e32 v4, v4
	v_add_f32_e32 v5, 1.0, v13
	v_rcp_f32_e32 v5, v5
	v_mul_f32_e32 v6, v8, v9
	v_mul_f32_e32 v8, v4, v6
	v_mul_f32_e32 v4, v10, v11
	v_mul_f32_e32 v9, v5, v4
	v_mov_b32_e32 v4, v96
	v_mov_b32_e32 v5, v92
	v_pk_mul_f32 v[4:5], v[4:5], s[18:19] op_sel_hi:[1,0]
	v_mov_b32_e32 v92, v97
	v_mul_f32_e32 v6, 0xbfb8aa3b, v4
	v_exp_f32_e32 v10, v6
	v_pk_mul_f32 v[6:7], v[92:93], s[18:19] op_sel_hi:[1,0]
	v_mul_f32_e32 v12, v4, v5
	v_mul_f32_e32 v11, 0xbfb8aa3b, v6
	v_exp_f32_e32 v11, v11
	v_add_f32_e32 v4, 1.0, v10
	v_rcp_f32_e32 v10, v4
	v_mov_b32_e32 v5, v82
	v_add_f32_e32 v4, 1.0, v11
	v_rcp_f32_e32 v11, v4
	v_mov_b32_e32 v4, v86
	v_pk_mul_f32 v[4:5], v[4:5], s[18:19] op_sel_hi:[1,0]
	v_mul_f32_e32 v6, v6, v7
	v_mul_f32_e32 v13, 0xbfb8aa3b, v4
	v_exp_f32_e32 v13, v13
	v_mul_f32_e32 v11, v11, v6
	v_mov_b32_e32 v82, v87
	v_mul_f32_e32 v10, v10, v12
	v_add_f32_e32 v6, 1.0, v13
	v_rcp_f32_e32 v12, v6
	v_pk_mul_f32 v[6:7], v[82:83], s[18:19] op_sel_hi:[1,0]
	v_mul_f32_e32 v4, v4, v5
	v_mul_f32_e32 v13, 0xbfb8aa3b, v6
	v_exp_f32_e32 v13, v13
	v_mul_f32_e32 v12, v12, v4
	v_mov_b32_e32 v5, v84
	v_mul_f32_e32 v14, v6, v7
	v_add_f32_e32 v4, 1.0, v13
	v_rcp_f32_e32 v13, v4
	v_mov_b32_e32 v4, v88
	v_pk_mul_f32 v[4:5], v[4:5], s[18:19] op_sel_hi:[1,0]
	v_mov_b32_e32 v84, v89
	v_mul_f32_e32 v6, 0xbfb8aa3b, v4
	v_exp_f32_e32 v15, v6
	v_pk_mul_f32 v[6:7], v[84:85], s[18:19] op_sel_hi:[1,0]
	v_mul_f32_e32 v13, v13, v14
	v_mul_f32_e32 v16, 0xbfb8aa3b, v6
	v_exp_f32_e32 v16, v16
	v_add_f32_e32 v14, 1.0, v15
	v_rcp_f32_e32 v14, v14
	v_mul_f32_e32 v4, v4, v5
	v_add_f32_e32 v15, 1.0, v16
	v_rcp_f32_e32 v15, v15
	v_mul_f32_e32 v5, v6, v7
	v_mul_f32_e32 v4, v14, v4
	v_mul_f32_e32 v6, 4.0, v8
	v_mul_f32_e32 v5, v15, v5
	v_mul_f32_e32 v7, 4.0, v9
	v_mul_f32_e32 v8, 4.0, v10
	v_mul_f32_e32 v9, 4.0, v11
	v_mul_f32_e32 v10, 4.0, v12
	v_mul_f32_e32 v11, 4.0, v13
	v_mul_f32_e32 v12, 4.0, v4
	v_mul_f32_e32 v13, 4.0, v5
	v_med3_f32 v5, v6, s41, v205
	v_med3_f32 v6, v7, s41, v205
	v_mov_b32_e32 v4, v163
	v_cvt_pk_fp8_f32 v4, v5, v6
	v_med3_f32 v6, v8, s41, v205
	v_med3_f32 v7, v9, s41, v205
	v_med3_f32 v8, v10, s41, v205
	v_med3_f32 v9, v11, s41, v205
	v_mov_b32_e32 v5, v163
	v_cvt_pk_fp8_f32 v5, v8, v9
	v_mov_b32_e32 v8, v78
	v_mov_b32_e32 v9, v74
	v_pk_mul_f32 v[8:9], v[8:9], s[18:19] op_sel_hi:[1,0]
	v_mov_b32_e32 v74, v79
	v_mul_f32_e32 v10, 0xbfb8aa3b, v8
	v_cvt_pk_fp8_f32 v4, v6, v7 op_sel:[0,0,1]
	v_med3_f32 v6, v12, s41, v205
	v_med3_f32 v7, v13, s41, v205
	v_exp_f32_e32 v12, v10
	v_pk_mul_f32 v[10:11], v[74:75], s[18:19] op_sel_hi:[1,0]
	v_cvt_pk_fp8_f32 v5, v6, v7 op_sel:[0,0,1]
	v_mul_f32_e32 v13, 0xbfb8aa3b, v10
	v_exp_f32_e32 v13, v13
	v_add_co_u32_e32 v6, vcc, s42, v2
	v_mov_b32_e32 v182, v176
	s_nop 0
	v_addc_co_u32_e32 v7, vcc, 0, v3, vcc
	global_store_dwordx2 v[6:7], v[4:5], off
	v_add_f32_e32 v4, 1.0, v12
	v_rcp_f32_e32 v4, v4
	v_add_f32_e32 v5, 1.0, v13
	v_rcp_f32_e32 v5, v5
	v_mul_f32_e32 v6, v8, v9
	v_mul_f32_e32 v8, v4, v6
	v_mul_f32_e32 v4, v10, v11
	v_mul_f32_e32 v9, v5, v4
	v_mov_b32_e32 v4, v80
	v_mov_b32_e32 v5, v76
	v_pk_mul_f32 v[4:5], v[4:5], s[18:19] op_sel_hi:[1,0]
	v_mov_b32_e32 v76, v81
	v_mul_f32_e32 v6, 0xbfb8aa3b, v4
	v_exp_f32_e32 v10, v6
	v_pk_mul_f32 v[6:7], v[76:77], s[18:19] op_sel_hi:[1,0]
	v_mul_f32_e32 v12, v4, v5
	v_mul_f32_e32 v11, 0xbfb8aa3b, v6
	v_exp_f32_e32 v11, v11
	v_add_f32_e32 v4, 1.0, v10
	v_rcp_f32_e32 v10, v4
	v_mov_b32_e32 v5, v66
	v_add_f32_e32 v4, 1.0, v11
	v_rcp_f32_e32 v11, v4
	v_mov_b32_e32 v4, v70
	v_pk_mul_f32 v[4:5], v[4:5], s[18:19] op_sel_hi:[1,0]
	v_mul_f32_e32 v6, v6, v7
	v_mul_f32_e32 v13, 0xbfb8aa3b, v4
	v_exp_f32_e32 v13, v13
	v_mul_f32_e32 v11, v11, v6
	v_mov_b32_e32 v66, v71
	v_mul_f32_e32 v10, v10, v12
	v_add_f32_e32 v6, 1.0, v13
	v_rcp_f32_e32 v12, v6
	v_pk_mul_f32 v[6:7], v[66:67], s[18:19] op_sel_hi:[1,0]
	v_mul_f32_e32 v4, v4, v5
	v_mul_f32_e32 v13, 0xbfb8aa3b, v6
	v_exp_f32_e32 v13, v13
	v_mul_f32_e32 v12, v12, v4
	v_mov_b32_e32 v5, v68
	v_mul_f32_e32 v14, v6, v7
	v_add_f32_e32 v4, 1.0, v13
	v_rcp_f32_e32 v13, v4
	v_mov_b32_e32 v4, v72
	v_pk_mul_f32 v[4:5], v[4:5], s[18:19] op_sel_hi:[1,0]
	v_mov_b32_e32 v68, v73
	v_mul_f32_e32 v6, 0xbfb8aa3b, v4
	v_exp_f32_e32 v15, v6
	v_pk_mul_f32 v[6:7], v[68:69], s[18:19] op_sel_hi:[1,0]
	v_mul_f32_e32 v13, v13, v14
	v_mul_f32_e32 v16, 0xbfb8aa3b, v6
	v_exp_f32_e32 v16, v16
	v_add_f32_e32 v14, 1.0, v15
	v_rcp_f32_e32 v14, v14
	v_mul_f32_e32 v4, v4, v5
	v_add_f32_e32 v15, 1.0, v16
	v_rcp_f32_e32 v15, v15
	v_mul_f32_e32 v5, v6, v7
	v_mul_f32_e32 v4, v14, v4
	v_mul_f32_e32 v6, 4.0, v8
	v_mul_f32_e32 v5, v15, v5
	v_mul_f32_e32 v7, 4.0, v9
	v_mul_f32_e32 v8, 4.0, v10
	v_mul_f32_e32 v9, 4.0, v11
	v_mul_f32_e32 v10, 4.0, v12
	v_mul_f32_e32 v11, 4.0, v13
	v_mul_f32_e32 v12, 4.0, v4
	v_mul_f32_e32 v13, 4.0, v5
	v_med3_f32 v5, v6, s41, v205
	v_med3_f32 v6, v7, s41, v205
	v_mov_b32_e32 v4, v163
	v_cvt_pk_fp8_f32 v4, v5, v6
	v_med3_f32 v6, v8, s41, v205
	v_med3_f32 v7, v9, s41, v205
	v_med3_f32 v8, v10, s41, v205
	v_med3_f32 v9, v11, s41, v205
	v_mov_b32_e32 v5, v163
	v_cvt_pk_fp8_f32 v5, v8, v9
	v_mov_b32_e32 v8, v62
	v_mov_b32_e32 v9, v58
	v_pk_mul_f32 v[8:9], v[8:9], s[18:19] op_sel_hi:[1,0]
	v_mov_b32_e32 v58, v63
	v_mul_f32_e32 v10, 0xbfb8aa3b, v8
	v_cvt_pk_fp8_f32 v4, v6, v7 op_sel:[0,0,1]
	v_med3_f32 v6, v12, s41, v205
	v_med3_f32 v7, v13, s41, v205
	v_exp_f32_e32 v12, v10
	v_pk_mul_f32 v[10:11], v[58:59], s[18:19] op_sel_hi:[1,0]
	v_cvt_pk_fp8_f32 v5, v6, v7 op_sel:[0,0,1]
	v_mul_f32_e32 v13, 0xbfb8aa3b, v10
	v_exp_f32_e32 v13, v13
	v_add_co_u32_e32 v6, vcc, s43, v2
	v_mov_b32_e32 v180, v174
	s_nop 0
	v_addc_co_u32_e32 v7, vcc, 0, v3, vcc
	global_store_dwordx2 v[6:7], v[4:5], off
	v_add_f32_e32 v4, 1.0, v12
	v_rcp_f32_e32 v4, v4
	v_add_f32_e32 v5, 1.0, v13
	v_rcp_f32_e32 v5, v5
	v_mul_f32_e32 v6, v8, v9
	v_mul_f32_e32 v8, v4, v6
	v_mul_f32_e32 v4, v10, v11
	v_mul_f32_e32 v9, v5, v4
	v_mov_b32_e32 v4, v64
	v_mov_b32_e32 v5, v60
	v_pk_mul_f32 v[4:5], v[4:5], s[18:19] op_sel_hi:[1,0]
	v_mov_b32_e32 v60, v65
	v_mul_f32_e32 v6, 0xbfb8aa3b, v4
	v_exp_f32_e32 v10, v6
	v_pk_mul_f32 v[6:7], v[60:61], s[18:19] op_sel_hi:[1,0]
	v_mul_f32_e32 v12, v4, v5
	v_mul_f32_e32 v11, 0xbfb8aa3b, v6
	v_exp_f32_e32 v11, v11
	v_add_f32_e32 v4, 1.0, v10
	v_rcp_f32_e32 v10, v4
	v_mov_b32_e32 v5, v50
	v_add_f32_e32 v4, 1.0, v11
	v_rcp_f32_e32 v11, v4
	v_mov_b32_e32 v4, v54
	v_pk_mul_f32 v[4:5], v[4:5], s[18:19] op_sel_hi:[1,0]
	v_mul_f32_e32 v6, v6, v7
	v_mul_f32_e32 v13, 0xbfb8aa3b, v4
	v_exp_f32_e32 v13, v13
	v_mul_f32_e32 v11, v11, v6
	v_mov_b32_e32 v50, v55
	v_mul_f32_e32 v10, v10, v12
	v_add_f32_e32 v6, 1.0, v13
	v_rcp_f32_e32 v12, v6
	v_pk_mul_f32 v[6:7], v[50:51], s[18:19] op_sel_hi:[1,0]
	v_mul_f32_e32 v4, v4, v5
	v_mul_f32_e32 v13, 0xbfb8aa3b, v6
	v_exp_f32_e32 v13, v13
	v_mul_f32_e32 v12, v12, v4
	v_mov_b32_e32 v5, v52
	v_mul_f32_e32 v14, v6, v7
	v_add_f32_e32 v4, 1.0, v13
	v_rcp_f32_e32 v13, v4
	v_mov_b32_e32 v4, v56
	v_pk_mul_f32 v[4:5], v[4:5], s[18:19] op_sel_hi:[1,0]
	v_mov_b32_e32 v52, v57
	v_mul_f32_e32 v6, 0xbfb8aa3b, v4
	v_exp_f32_e32 v15, v6
	v_pk_mul_f32 v[6:7], v[52:53], s[18:19] op_sel_hi:[1,0]
	v_mul_f32_e32 v13, v13, v14
	v_mul_f32_e32 v16, 0xbfb8aa3b, v6
	v_exp_f32_e32 v16, v16
	v_add_f32_e32 v14, 1.0, v15
	v_rcp_f32_e32 v14, v14
	v_mul_f32_e32 v4, v4, v5
	v_add_f32_e32 v15, 1.0, v16
	v_rcp_f32_e32 v15, v15
	v_mul_f32_e32 v5, v6, v7
	v_mul_f32_e32 v4, v14, v4
	v_mul_f32_e32 v6, 4.0, v8
	v_mul_f32_e32 v5, v15, v5
	v_mul_f32_e32 v7, 4.0, v9
	v_mul_f32_e32 v8, 4.0, v10
	v_mul_f32_e32 v9, 4.0, v11
	v_mul_f32_e32 v10, 4.0, v12
	v_mul_f32_e32 v11, 4.0, v13
	v_mul_f32_e32 v12, 4.0, v4
	v_mul_f32_e32 v13, 4.0, v5
	v_med3_f32 v5, v6, s41, v205
	v_med3_f32 v6, v7, s41, v205
	v_mov_b32_e32 v4, v163
	v_cvt_pk_fp8_f32 v4, v5, v6
	v_med3_f32 v6, v8, s41, v205
	v_med3_f32 v7, v9, s41, v205
	v_med3_f32 v8, v10, s41, v205
	v_med3_f32 v9, v11, s41, v205
	v_mov_b32_e32 v5, v163
	v_cvt_pk_fp8_f32 v5, v8, v9
	v_mov_b32_e32 v8, v46
	v_mov_b32_e32 v9, v42
	v_pk_mul_f32 v[8:9], v[8:9], s[18:19] op_sel_hi:[1,0]
	v_mov_b32_e32 v42, v47
	v_mul_f32_e32 v10, 0xbfb8aa3b, v8
	v_cvt_pk_fp8_f32 v4, v6, v7 op_sel:[0,0,1]
	v_med3_f32 v6, v12, s41, v205
	v_med3_f32 v7, v13, s41, v205
	v_exp_f32_e32 v12, v10
	v_pk_mul_f32 v[10:11], v[42:43], s[18:19] op_sel_hi:[1,0]
	v_cvt_pk_fp8_f32 v5, v6, v7 op_sel:[0,0,1]
	v_mul_f32_e32 v13, 0xbfb8aa3b, v10
	v_exp_f32_e32 v13, v13
	v_add_co_u32_e32 v6, vcc, s44, v2
	v_mov_b32_e32 v178, v207
	s_nop 0
	v_addc_co_u32_e32 v7, vcc, 0, v3, vcc
	global_store_dwordx2 v[6:7], v[4:5], off
	v_add_f32_e32 v4, 1.0, v12
	v_rcp_f32_e32 v4, v4
	v_add_f32_e32 v5, 1.0, v13
	v_rcp_f32_e32 v5, v5
	v_mul_f32_e32 v6, v8, v9
	v_mul_f32_e32 v8, v4, v6
	v_mul_f32_e32 v4, v10, v11
	v_mul_f32_e32 v9, v5, v4
	v_mov_b32_e32 v4, v48
	v_mov_b32_e32 v5, v44
	v_pk_mul_f32 v[4:5], v[4:5], s[18:19] op_sel_hi:[1,0]
	v_mov_b32_e32 v44, v49
	v_mul_f32_e32 v6, 0xbfb8aa3b, v4
	v_exp_f32_e32 v10, v6
	v_pk_mul_f32 v[6:7], v[44:45], s[18:19] op_sel_hi:[1,0]
	v_mul_f32_e32 v12, v4, v5
	v_mul_f32_e32 v11, 0xbfb8aa3b, v6
	v_exp_f32_e32 v11, v11
	v_add_f32_e32 v4, 1.0, v10
	v_rcp_f32_e32 v10, v4
	v_mov_b32_e32 v5, v34
	v_add_f32_e32 v4, 1.0, v11
	v_rcp_f32_e32 v11, v4
	v_mov_b32_e32 v4, v38
	v_pk_mul_f32 v[4:5], v[4:5], s[18:19] op_sel_hi:[1,0]
	v_mul_f32_e32 v6, v6, v7
	v_mul_f32_e32 v13, 0xbfb8aa3b, v4
	v_exp_f32_e32 v13, v13
	v_mul_f32_e32 v11, v11, v6
	v_mov_b32_e32 v34, v39
	v_mul_f32_e32 v10, v10, v12
	v_add_f32_e32 v6, 1.0, v13
	v_rcp_f32_e32 v12, v6
	v_pk_mul_f32 v[6:7], v[34:35], s[18:19] op_sel_hi:[1,0]
	v_mul_f32_e32 v4, v4, v5
	v_mul_f32_e32 v13, 0xbfb8aa3b, v6
	v_exp_f32_e32 v13, v13
	v_mul_f32_e32 v12, v12, v4
	v_mov_b32_e32 v5, v36
	v_mul_f32_e32 v14, v6, v7
	v_add_f32_e32 v4, 1.0, v13
	v_rcp_f32_e32 v13, v4
	v_mov_b32_e32 v4, v40
	v_pk_mul_f32 v[4:5], v[4:5], s[18:19] op_sel_hi:[1,0]
	v_mov_b32_e32 v36, v41
	v_mul_f32_e32 v6, 0xbfb8aa3b, v4
	v_exp_f32_e32 v15, v6
	v_pk_mul_f32 v[6:7], v[36:37], s[18:19] op_sel_hi:[1,0]
	v_mul_f32_e32 v13, v13, v14
	v_mul_f32_e32 v16, 0xbfb8aa3b, v6
	v_exp_f32_e32 v16, v16
	v_add_f32_e32 v14, 1.0, v15
	v_rcp_f32_e32 v14, v14
	v_mul_f32_e32 v4, v4, v5
	v_add_f32_e32 v15, 1.0, v16
	v_rcp_f32_e32 v15, v15
	v_mul_f32_e32 v5, v6, v7
	v_mul_f32_e32 v4, v14, v4
	v_mul_f32_e32 v6, 4.0, v8
	v_mul_f32_e32 v5, v15, v5
	v_mul_f32_e32 v7, 4.0, v9
	v_mul_f32_e32 v8, 4.0, v10
	v_mul_f32_e32 v9, 4.0, v11
	v_mul_f32_e32 v10, 4.0, v12
	v_mul_f32_e32 v11, 4.0, v13
	v_mul_f32_e32 v12, 4.0, v4
	v_mul_f32_e32 v13, 4.0, v5
	v_med3_f32 v5, v6, s41, v205
	v_med3_f32 v6, v7, s41, v205
	v_mov_b32_e32 v4, v163
	v_cvt_pk_fp8_f32 v4, v5, v6
	v_med3_f32 v6, v8, s41, v205
	v_med3_f32 v7, v9, s41, v205
	v_med3_f32 v8, v10, s41, v205
	v_med3_f32 v9, v11, s41, v205
	v_mov_b32_e32 v5, v163
	v_cvt_pk_fp8_f32 v5, v8, v9
	v_cvt_pk_fp8_f32 v4, v6, v7 op_sel:[0,0,1]
	v_med3_f32 v6, v12, s41, v205
	v_med3_f32 v7, v13, s41, v205
	v_cvt_pk_fp8_f32 v5, v6, v7 op_sel:[0,0,1]
	v_add_co_u32_e32 v2, vcc, 0x58000, v2
	v_mov_b32_e32 v208, v206
	s_nop 0
	v_addc_co_u32_e32 v3, vcc, 0, v3, vcc
	s_and_b64 vcc, exec, s[0:1]
	s_mov_b32 s48, s47
	s_mov_b32 s22, s20
	s_mov_b64 s[24:25], s[6:7]
	s_mov_b32 s21, s45
	global_store_dwordx2 v[2:3], v[4:5], off
	s_cbranch_vccz .LBB0_1042
	s_waitcnt vmcnt(0)
	s_cmpk_gt_u32 s19, 0xff
	s_cbranch_scc1 .LBB0_1064
	s_barrier

.LBB0_1128:
	s_add_u32 s34, s30, 0xfffc0080
	s_addc_u32 s35, s31, -1
	s_cmp_eq_u32 s60, 12
	s_cselect_b32 s37, s19, s35
	s_cselect_b32 s36, s56, s34
	s_cselect_b32 s35, s21, s59
	s_cselect_b32 s34, s57, s58
	v_lshl_add_u64 v[164:165], s[30:31], 0, v[156:157]
	s_add_i32 m0, s27, 0xc000
	ds_read_b128 v[184:187], v177
	ds_read_b128 v[188:191], v177 offset:1024
	ds_read_b128 v[198:201], v177 offset:2048
	ds_read_b128 v[202:205], v177 offset:3072
	ds_read_b128 v[206:209], v177 offset:4096
	ds_read_b128 v[210:213], v177 offset:5120
	ds_read_b128 v[214:217], v177 offset:6144
	ds_read_b128 v[218:221], v177 offset:7168
	global_load_lds_dwordx4 v[164:165], off
	v_lshl_add_u64 v[164:165], s[30:31], 0, v[158:159]
	s_add_i32 m0, s27, 0xe000
	s_nop 0
	global_load_lds_dwordx4 v[164:165], off
	s_waitcnt lgkmcnt(8)
	s_barrier
	s_waitcnt lgkmcnt(0)
	s_waitcnt lgkmcnt(0)
	v_mfma_f32_16x16x128_f8f6f4 v[142:145], v[2:9], v[184:191], v[142:145]
	v_mfma_f32_16x16x128_f8f6f4 v[138:141], v[10:17], v[184:191], v[138:141]
	v_mfma_f32_16x16x128_f8f6f4 v[126:129], v[2:9], v[198:205], v[126:129]
	v_mfma_f32_16x16x128_f8f6f4 v[122:125], v[10:17], v[198:205], v[122:125]
	v_mfma_f32_16x16x128_f8f6f4 v[110:113], v[2:9], v[206:213], v[110:113]
	v_mfma_f32_16x16x128_f8f6f4 v[106:109], v[10:17], v[206:213], v[106:109]
	v_mfma_f32_16x16x128_f8f6f4 v[94:97], v[2:9], v[214:221], v[94:97]
	v_mfma_f32_16x16x128_f8f6f4 v[90:93], v[10:17], v[214:221], v[90:93]
	s_barrier
	s_add_i32 s61, s50, s42
	v_lshl_add_u64 v[164:165], s[34:35], 0, v[148:149]
	s_mov_b32 m0, s61
	ds_read_b128 v[222:225], v178
	ds_read_b128 v[226:229], v178 offset:1024
	ds_read_b128 v[230:233], v178 offset:2048
	ds_read_b128 v[234:237], v178 offset:3072
	global_load_lds_dwordx4 v[164:165], off
	v_lshl_add_u64 v[166:167], s[34:35], 0, v[152:153]
	s_add_i32 m0, s61, 0x2000
	s_nop 0
	global_load_lds_dwordx4 v[166:167], off
	s_barrier
	s_waitcnt lgkmcnt(0)
	s_waitcnt lgkmcnt(0)
	v_mfma_f32_16x16x128_f8f6f4 v[134:137], v[222:229], v[184:191], v[134:137]
	v_mfma_f32_16x16x128_f8f6f4 v[130:133], v[230:237], v[184:191], v[130:133]
	v_mfma_f32_16x16x128_f8f6f4 v[118:121], v[222:229], v[198:205], v[118:121]
	v_mfma_f32_16x16x128_f8f6f4 v[114:117], v[230:237], v[198:205], v[114:117]
	v_mfma_f32_16x16x128_f8f6f4 v[102:105], v[222:229], v[206:213], v[102:105]
	v_mfma_f32_16x16x128_f8f6f4 v[98:101], v[230:237], v[206:213], v[98:101]
	v_mfma_f32_16x16x128_f8f6f4 v[86:89], v[222:229], v[214:221], v[86:89]
	v_mfma_f32_16x16x128_f8f6f4 v[82:85], v[230:237], v[214:221], v[82:85]
	s_mov_b32 m0, s27
	v_lshl_add_u64 v[168:169], s[36:37], 0, v[146:147]
	s_barrier
	ds_read_b128 v[184:187], v177 offset:16384
	ds_read_b128 v[188:191], v177 offset:17408
	ds_read_b128 v[198:201], v177 offset:18432
	ds_read_b128 v[202:205], v177 offset:19456
	ds_read_b128 v[206:209], v177 offset:20480
	ds_read_b128 v[210:213], v177 offset:21504
	ds_read_b128 v[214:217], v177 offset:22528
	ds_read_b128 v[218:221], v177 offset:23552
	global_load_lds_dwordx4 v[168:169], off
	v_lshl_add_u64 v[170:171], s[36:37], 0, v[150:151]
	s_mov_b32 m0, s29
	s_nop 0
	global_load_lds_dwordx4 v[170:171], off
	s_waitcnt vmcnt(10)
	s_barrier
	s_waitcnt lgkmcnt(0)
	s_waitcnt lgkmcnt(0)
	v_mfma_f32_16x16x128_f8f6f4 v[78:81], v[2:9], v[184:191], v[78:81]
	v_mfma_f32_16x16x128_f8f6f4 v[74:77], v[10:17], v[184:191], v[74:77]
	v_mfma_f32_16x16x128_f8f6f4 v[66:69], v[2:9], v[198:205], v[66:69]
	v_mfma_f32_16x16x128_f8f6f4 v[58:61], v[10:17], v[198:205], v[58:61]
	v_mfma_f32_16x16x128_f8f6f4 v[50:53], v[2:9], v[206:213], v[50:53]
	v_mfma_f32_16x16x128_f8f6f4 v[42:45], v[10:17], v[206:213], v[42:45]
	v_mfma_f32_16x16x128_f8f6f4 v[34:37], v[2:9], v[214:221], v[34:37]
	v_mfma_f32_16x16x128_f8f6f4 v[26:29], v[10:17], v[214:221], v[26:29]
	s_barrier
	ds_read_b128 v[2:5], v176 offset:32768
	ds_read_b128 v[6:9], v176 offset:33792
	ds_read_b128 v[10:13], v176 offset:34816
	ds_read_b128 v[14:17], v176 offset:35840
	s_add_u32 s64, s34, 0x40000
	s_addc_u32 s65, s35, 0
	s_add_i32 s61, s51, s42
	v_lshl_add_u64 v[238:239], s[64:65], 0, v[148:149]
	s_mov_b32 m0, s61
	s_nop 0
	global_load_lds_dwordx4 v[238:239], off
	v_lshl_add_u64 v[238:239], s[64:65], 0, v[152:153]
	s_add_i32 m0, s61, 0x2000
	s_nop 0
	global_load_lds_dwordx4 v[238:239], off
	s_waitcnt vmcnt(6)
	s_barrier
	v_mfma_f32_16x16x128_f8f6f4 v[70:73], v[222:229], v[184:191], v[70:73]
	v_mfma_f32_16x16x128_f8f6f4 v[62:65], v[230:237], v[184:191], v[62:65]
	v_mfma_f32_16x16x128_f8f6f4 v[54:57], v[222:229], v[198:205], v[54:57]
	v_mfma_f32_16x16x128_f8f6f4 v[46:49], v[230:237], v[198:205], v[46:49]
	v_mfma_f32_16x16x128_f8f6f4 v[38:41], v[222:229], v[206:213], v[38:41]
	v_mfma_f32_16x16x128_f8f6f4 v[30:33], v[230:237], v[206:213], v[30:33]
	v_mfma_f32_16x16x128_f8f6f4 v[22:25], v[222:229], v[214:221], v[22:25]
	v_mfma_f32_16x16x128_f8f6f4 v[18:21], v[230:237], v[214:221], v[18:21]
	s_add_i32 s61, 0, 0x18000
	s_barrier
	s_add_u32 s36, s36, 0x40000
	s_addc_u32 s37, s37, 0
	s_mov_b32 m0, s44
	v_lshl_add_u64 v[192:193], s[36:37], 0, v[146:147]
	ds_read_b128 v[184:187], v177 offset:32768
	ds_read_b128 v[188:191], v177 offset:33792
	ds_read_b128 v[198:201], v177 offset:34816
	ds_read_b128 v[202:205], v177 offset:35840
	ds_read_b128 v[206:209], v177 offset:36864
	ds_read_b128 v[210:213], v177 offset:37888
	ds_read_b128 v[214:217], v177 offset:38912
	ds_read_b128 v[218:221], v177 offset:39936
	global_load_lds_dwordx4 v[192:193], off
	v_lshl_add_u64 v[192:193], s[36:37], 0, v[150:151]
	s_mov_b32 m0, s45
	s_nop 0
	global_load_lds_dwordx4 v[192:193], off
	s_waitcnt lgkmcnt(8)
	s_barrier
	s_waitcnt lgkmcnt(0)
	s_waitcnt lgkmcnt(0)
	v_mfma_f32_16x16x128_f8f6f4 v[142:145], v[2:9], v[184:191], v[142:145]
	v_mfma_f32_16x16x128_f8f6f4 v[138:141], v[10:17], v[184:191], v[138:141]
	v_mfma_f32_16x16x128_f8f6f4 v[126:129], v[2:9], v[198:205], v[126:129]
	v_mfma_f32_16x16x128_f8f6f4 v[122:125], v[10:17], v[198:205], v[122:125]
	v_mfma_f32_16x16x128_f8f6f4 v[110:113], v[2:9], v[206:213], v[110:113]
	v_mfma_f32_16x16x128_f8f6f4 v[106:109], v[10:17], v[206:213], v[106:109]
	v_mfma_f32_16x16x128_f8f6f4 v[94:97], v[2:9], v[214:221], v[94:97]
	v_mfma_f32_16x16x128_f8f6f4 v[90:93], v[10:17], v[214:221], v[90:93]
	s_barrier
	s_add_i32 s36, 0, 0x1c000
	s_add_i32 s37, s61, s42
	v_add_u32_e32 v192, s36, v174
	s_add_i32 m0, s37, 0xffffff80
	ds_read_b128 v[222:225], v192
	ds_read_b128 v[226:229], v192 offset:1024
	ds_read_b128 v[230:233], v192 offset:2048
	ds_read_b128 v[234:237], v192 offset:3072
	global_load_lds_dwordx4 v[164:165], off offset:128
	s_add_i32 m0, s37, 0x1f80
	s_nop 0
	global_load_lds_dwordx4 v[166:167], off offset:128
	s_barrier
	s_waitcnt lgkmcnt(0)
	s_waitcnt lgkmcnt(0)
	v_mfma_f32_16x16x128_f8f6f4 v[134:137], v[222:229], v[184:191], v[134:137]
	v_mfma_f32_16x16x128_f8f6f4 v[130:133], v[230:237], v[184:191], v[130:133]
	v_mfma_f32_16x16x128_f8f6f4 v[118:121], v[222:229], v[198:205], v[118:121]
	v_mfma_f32_16x16x128_f8f6f4 v[114:117], v[230:237], v[198:205], v[114:117]
	v_mfma_f32_16x16x128_f8f6f4 v[102:105], v[222:229], v[206:213], v[102:105]
	v_mfma_f32_16x16x128_f8f6f4 v[98:101], v[230:237], v[206:213], v[98:101]
	v_mfma_f32_16x16x128_f8f6f4 v[86:89], v[222:229], v[214:221], v[86:89]
	v_mfma_f32_16x16x128_f8f6f4 v[82:85], v[230:237], v[214:221], v[82:85]
	s_add_i32 m0, s48, 0xffffff80
	s_barrier
	ds_read_b128 v[184:187], v177 offset:49152
	ds_read_b128 v[188:191], v177 offset:50176
	ds_read_b128 v[198:201], v177 offset:51200
	ds_read_b128 v[202:205], v177 offset:52224
	ds_read_b128 v[206:209], v177 offset:53248
	ds_read_b128 v[210:213], v177 offset:54272
	ds_read_b128 v[214:217], v177 offset:55296
	ds_read_b128 v[218:221], v177 offset:56320
	global_load_lds_dwordx4 v[168:169], off offset:128
	s_add_i32 m0, s49, 0xffffff80
	s_nop 0
	global_load_lds_dwordx4 v[170:171], off offset:128
	s_waitcnt vmcnt(10)
	s_barrier
	s_waitcnt lgkmcnt(0)
	s_waitcnt lgkmcnt(0)
	v_mfma_f32_16x16x128_f8f6f4 v[78:81], v[2:9], v[184:191], v[78:81]
	v_mfma_f32_16x16x128_f8f6f4 v[74:77], v[10:17], v[184:191], v[74:77]
	v_mfma_f32_16x16x128_f8f6f4 v[66:69], v[2:9], v[198:205], v[66:69]
	v_mfma_f32_16x16x128_f8f6f4 v[58:61], v[10:17], v[198:205], v[58:61]
	v_mfma_f32_16x16x128_f8f6f4 v[50:53], v[2:9], v[206:213], v[50:53]
	v_mfma_f32_16x16x128_f8f6f4 v[42:45], v[10:17], v[206:213], v[42:45]
	v_mfma_f32_16x16x128_f8f6f4 v[34:37], v[2:9], v[214:221], v[34:37]
	v_mfma_f32_16x16x128_f8f6f4 v[26:29], v[10:17], v[214:221], v[26:29]
	s_barrier
	ds_read_b128 v[2:5], v176
	ds_read_b128 v[6:9], v176 offset:1024
	ds_read_b128 v[10:13], v176 offset:2048
	ds_read_b128 v[14:17], v176 offset:3072
	s_add_u32 s34, s34, 0x40080
	s_addc_u32 s35, s35, 0
	s_add_i32 s36, s36, s42
	v_lshl_add_u64 v[238:239], s[34:35], 0, v[148:149]
	s_mov_b32 m0, s36
	s_nop 0
	global_load_lds_dwordx4 v[238:239], off
	v_lshl_add_u64 v[238:239], s[34:35], 0, v[152:153]
	s_add_i32 m0, s36, 0x2000
	s_nop 0
	global_load_lds_dwordx4 v[238:239], off
	s_waitcnt vmcnt(6)
	s_barrier
	v_mfma_f32_16x16x128_f8f6f4 v[70:73], v[222:229], v[184:191], v[70:73]
	v_mfma_f32_16x16x128_f8f6f4 v[62:65], v[230:237], v[184:191], v[62:65]
	v_mfma_f32_16x16x128_f8f6f4 v[54:57], v[222:229], v[198:205], v[54:57]
	v_mfma_f32_16x16x128_f8f6f4 v[46:49], v[230:237], v[198:205], v[46:49]
	v_mfma_f32_16x16x128_f8f6f4 v[38:41], v[222:229], v[206:213], v[38:41]
	v_mfma_f32_16x16x128_f8f6f4 v[30:33], v[230:237], v[206:213], v[30:33]
	v_mfma_f32_16x16x128_f8f6f4 v[22:25], v[222:229], v[214:221], v[22:25]
	v_mfma_f32_16x16x128_f8f6f4 v[18:21], v[230:237], v[214:221], v[18:21]
	s_add_i32 s60, s60, 2
	s_add_u32 s30, s30, 0x100
	s_addc_u32 s31, s31, 0
	s_add_u32 s58, s58, 0x100
	s_addc_u32 s59, s59, 0
	s_cmp_gt_u32 s60, 13
	s_barrier
	s_cbranch_scc0 .LBB0_1128
	s_waitcnt lgkmcnt(0)
	v_lshl_add_u32 v8, s26, 8, v172
	s_lshl_b32 s19, s28, 8
	s_and_b32 s19, s19, 0x700
	v_ashrrev_i32_e32 v9, 31, v8
	v_or_b32_e32 v4, s19, v175
	s_waitcnt vmcnt(0)
	v_mul_f32_e32 v10, 0x3b800000, v154
	v_lshlrev_b64 v[2:3], 12, v[8:9]
	v_lshl_add_u64 v[2:3], s[6:7], 0, v[2:3]
	v_lshlrev_b32_e32 v154, 1, v4
	v_pk_mul_f32 v[4:5], v[10:11], v[142:143] op_sel_hi:[0,1]
	s_nop 15
	s_nop 15
	v_lshl_add_u64 v[2:3], v[2:3], 0, v[154:155]
	v_pk_mul_f32 v[6:7], v[10:11], v[144:145] op_sel_hi:[0,1]
	v_cvt_pk_bf16_f32 v4, v4, v5
	v_cvt_pk_bf16_f32 v5, v6, v7
	v_pk_mul_f32 v[12:13], v[10:11], v[140:141] op_sel_hi:[0,1]
	v_pk_mul_f32 v[14:15], v[10:11], v[138:139] op_sel_hi:[0,1]
	v_cvt_pk_bf16_f32 v6, v14, v15
	v_cvt_pk_bf16_f32 v7, v12, v13
	global_store_dwordx4 v[2:3], v[4:7], off
	v_pk_mul_f32 v[12:13], v[10:11], v[132:133] op_sel_hi:[0,1]
	s_nop 0
	v_pk_mul_f32 v[4:5], v[10:11], v[134:135] op_sel_hi:[0,1]
	v_pk_mul_f32 v[6:7], v[10:11], v[136:137] op_sel_hi:[0,1]
	v_cvt_pk_bf16_f32 v4, v4, v5
	v_pk_mul_f32 v[10:11], v[10:11], v[130:131] op_sel_hi:[0,1]
	v_cvt_pk_bf16_f32 v5, v6, v7
	v_cvt_pk_bf16_f32 v6, v10, v11
	v_cvt_pk_bf16_f32 v7, v12, v13
	global_store_dwordx4 v[2:3], v[4:7], off offset:256
	v_mul_f32_e32 v10, 0x3b800000, v183
	v_pk_mul_f32 v[14:15], v[10:11], v[124:125] op_sel_hi:[0,1]
	v_or_b32_e32 v4, 16, v8
	v_ashrrev_i32_e32 v5, 31, v4
	v_lshlrev_b64 v[4:5], 12, v[4:5]
	v_lshl_add_u64 v[4:5], s[6:7], 0, v[4:5]
	v_lshl_add_u64 v[12:13], v[4:5], 0, v[154:155]
	v_pk_mul_f32 v[4:5], v[10:11], v[126:127] op_sel_hi:[0,1]
	v_pk_mul_f32 v[6:7], v[10:11], v[128:129] op_sel_hi:[0,1]
	v_cvt_pk_bf16_f32 v4, v4, v5
	v_cvt_pk_bf16_f32 v5, v6, v7
	v_pk_mul_f32 v[16:17], v[10:11], v[122:123] op_sel_hi:[0,1]
	v_cvt_pk_bf16_f32 v6, v16, v17
	v_cvt_pk_bf16_f32 v7, v14, v15
	global_store_dwordx4 v[12:13], v[4:7], off
	v_pk_mul_f32 v[14:15], v[10:11], v[116:117] op_sel_hi:[0,1]
	s_nop 0
	v_pk_mul_f32 v[4:5], v[10:11], v[118:119] op_sel_hi:[0,1]
	v_pk_mul_f32 v[6:7], v[10:11], v[120:121] op_sel_hi:[0,1]
	v_cvt_pk_bf16_f32 v4, v4, v5
	v_pk_mul_f32 v[10:11], v[10:11], v[114:115] op_sel_hi:[0,1]
	v_cvt_pk_bf16_f32 v5, v6, v7
	v_cvt_pk_bf16_f32 v6, v10, v11
	v_cvt_pk_bf16_f32 v7, v14, v15
	global_store_dwordx4 v[12:13], v[4:7], off offset:256
	v_mul_f32_e32 v10, 0x3b800000, v182
	v_pk_mul_f32 v[14:15], v[10:11], v[108:109] op_sel_hi:[0,1]
	v_or_b32_e32 v4, 32, v8
	v_ashrrev_i32_e32 v5, 31, v4
	v_lshlrev_b64 v[4:5], 12, v[4:5]
	v_lshl_add_u64 v[4:5], s[6:7], 0, v[4:5]
	v_lshl_add_u64 v[12:13], v[4:5], 0, v[154:155]
	v_pk_mul_f32 v[4:5], v[10:11], v[110:111] op_sel_hi:[0,1]
	v_pk_mul_f32 v[6:7], v[10:11], v[112:113] op_sel_hi:[0,1]
	v_cvt_pk_bf16_f32 v4, v4, v5
	v_cvt_pk_bf16_f32 v5, v6, v7
	v_pk_mul_f32 v[16:17], v[10:11], v[106:107] op_sel_hi:[0,1]
	v_cvt_pk_bf16_f32 v6, v16, v17
	v_cvt_pk_bf16_f32 v7, v14, v15
	global_store_dwordx4 v[12:13], v[4:7], off
	v_pk_mul_f32 v[14:15], v[10:11], v[100:101] op_sel_hi:[0,1]
	s_nop 0
	v_pk_mul_f32 v[4:5], v[10:11], v[102:103] op_sel_hi:[0,1]
	v_pk_mul_f32 v[6:7], v[10:11], v[104:105] op_sel_hi:[0,1]
	v_cvt_pk_bf16_f32 v4, v4, v5
	v_pk_mul_f32 v[10:11], v[10:11], v[98:99] op_sel_hi:[0,1]
	v_cvt_pk_bf16_f32 v5, v6, v7
	v_cvt_pk_bf16_f32 v6, v10, v11
	v_cvt_pk_bf16_f32 v7, v14, v15
	global_store_dwordx4 v[12:13], v[4:7], off offset:256
	s_nop 1
	v_or_b32_e32 v4, 48, v8
	v_ashrrev_i32_e32 v5, 31, v4
	v_lshlrev_b64 v[4:5], 12, v[4:5]
	v_mul_f32_e32 v8, 0x3b800000, v181
	v_lshl_add_u64 v[4:5], s[6:7], 0, v[4:5]
	v_lshl_add_u64 v[10:11], v[4:5], 0, v[154:155]
	v_pk_mul_f32 v[6:7], v[8:9], v[96:97] op_sel_hi:[0,1]
	v_pk_mul_f32 v[4:5], v[8:9], v[94:95] op_sel_hi:[0,1]
	v_pk_mul_f32 v[12:13], v[8:9], v[92:93] op_sel_hi:[0,1]
	v_pk_mul_f32 v[14:15], v[8:9], v[90:91] op_sel_hi:[0,1]
	v_cvt_pk_bf16_f32 v4, v4, v5
	v_cvt_pk_bf16_f32 v5, v6, v7
	v_cvt_pk_bf16_f32 v6, v14, v15
	v_cvt_pk_bf16_f32 v7, v12, v13
	global_store_dwordx4 v[10:11], v[4:7], off
	v_pk_mul_f32 v[12:13], v[8:9], v[84:85] op_sel_hi:[0,1]
	s_nop 0
	v_pk_mul_f32 v[6:7], v[8:9], v[88:89] op_sel_hi:[0,1]
	v_pk_mul_f32 v[4:5], v[8:9], v[86:87] op_sel_hi:[0,1]
	v_pk_mul_f32 v[8:9], v[8:9], v[82:83] op_sel_hi:[0,1]
	v_cvt_pk_bf16_f32 v4, v4, v5
	v_cvt_pk_bf16_f32 v5, v6, v7
	v_cvt_pk_bf16_f32 v6, v8, v9
	v_cvt_pk_bf16_f32 v7, v12, v13
	v_mul_f32_e32 v8, 0x3b800000, v180
	global_store_dwordx4 v[10:11], v[4:7], off offset:256
	v_pk_mul_f32 v[12:13], v[8:9], v[76:77] op_sel_hi:[0,1]
	v_pk_mul_f32 v[14:15], v[8:9], v[74:75] op_sel_hi:[0,1]
	v_pk_mul_f32 v[6:7], v[8:9], v[80:81] op_sel_hi:[0,1]
	v_pk_mul_f32 v[4:5], v[8:9], v[78:79] op_sel_hi:[0,1]
	v_cvt_pk_bf16_f32 v4, v4, v5
	v_cvt_pk_bf16_f32 v5, v6, v7
	v_cvt_pk_bf16_f32 v6, v14, v15
	v_cvt_pk_bf16_f32 v7, v12, v13
	v_add_co_u32_e32 v12, vcc, s52, v2
	v_lshl_add_u64 v[10:11], v[2:3], 0, s[10:11]
	s_nop 0
	v_addc_co_u32_e32 v13, vcc, 0, v3, vcc
	global_store_dwordx4 v[12:13], v[4:7], off
	v_pk_mul_f32 v[12:13], v[8:9], v[64:65] op_sel_hi:[0,1]
	s_nop 0
	v_pk_mul_f32 v[6:7], v[8:9], v[72:73] op_sel_hi:[0,1]
	v_pk_mul_f32 v[4:5], v[8:9], v[70:71] op_sel_hi:[0,1]
	v_pk_mul_f32 v[8:9], v[8:9], v[62:63] op_sel_hi:[0,1]
	v_cvt_pk_bf16_f32 v4, v4, v5
	v_cvt_pk_bf16_f32 v5, v6, v7
	v_cvt_pk_bf16_f32 v6, v8, v9
	v_cvt_pk_bf16_f32 v7, v12, v13
	v_mul_f32_e32 v8, 0x3b800000, v179
	global_store_dwordx4 v[10:11], v[4:7], off offset:256
	v_pk_mul_f32 v[12:13], v[8:9], v[60:61] op_sel_hi:[0,1]
	v_pk_mul_f32 v[14:15], v[8:9], v[58:59] op_sel_hi:[0,1]
	v_pk_mul_f32 v[6:7], v[8:9], v[68:69] op_sel_hi:[0,1]
	v_pk_mul_f32 v[4:5], v[8:9], v[66:67] op_sel_hi:[0,1]
	v_cvt_pk_bf16_f32 v4, v4, v5
	v_cvt_pk_bf16_f32 v5, v6, v7
	v_cvt_pk_bf16_f32 v6, v14, v15
	v_cvt_pk_bf16_f32 v7, v12, v13
	v_add_co_u32_e32 v12, vcc, s53, v2
	v_lshl_add_u64 v[10:11], v[2:3], 0, s[12:13]
	s_nop 0
	v_addc_co_u32_e32 v13, vcc, 0, v3, vcc
	global_store_dwordx4 v[12:13], v[4:7], off
	v_pk_mul_f32 v[12:13], v[8:9], v[48:49] op_sel_hi:[0,1]
	s_nop 0
	v_pk_mul_f32 v[6:7], v[8:9], v[56:57] op_sel_hi:[0,1]
	v_pk_mul_f32 v[4:5], v[8:9], v[54:55] op_sel_hi:[0,1]
	v_pk_mul_f32 v[8:9], v[8:9], v[46:47] op_sel_hi:[0,1]
	v_cvt_pk_bf16_f32 v4, v4, v5
	v_cvt_pk_bf16_f32 v5, v6, v7
	v_cvt_pk_bf16_f32 v6, v8, v9
	v_cvt_pk_bf16_f32 v7, v12, v13
	v_mul_f32_e32 v8, 0x3b800000, v173
	global_store_dwordx4 v[10:11], v[4:7], off offset:256
	v_pk_mul_f32 v[12:13], v[8:9], v[44:45] op_sel_hi:[0,1]
	v_pk_mul_f32 v[14:15], v[8:9], v[42:43] op_sel_hi:[0,1]
	v_pk_mul_f32 v[6:7], v[8:9], v[52:53] op_sel_hi:[0,1]
	v_pk_mul_f32 v[4:5], v[8:9], v[50:51] op_sel_hi:[0,1]
	v_cvt_pk_bf16_f32 v4, v4, v5
	v_cvt_pk_bf16_f32 v5, v6, v7
	v_cvt_pk_bf16_f32 v6, v14, v15
	v_cvt_pk_bf16_f32 v7, v12, v13
	v_add_co_u32_e32 v12, vcc, s54, v2
	v_lshl_add_u64 v[10:11], v[2:3], 0, s[14:15]
	s_nop 0
	v_addc_co_u32_e32 v13, vcc, 0, v3, vcc
	global_store_dwordx4 v[12:13], v[4:7], off
	v_pk_mul_f32 v[12:13], v[8:9], v[32:33] op_sel_hi:[0,1]
	s_nop 0
	v_pk_mul_f32 v[6:7], v[8:9], v[40:41] op_sel_hi:[0,1]
	v_pk_mul_f32 v[4:5], v[8:9], v[38:39] op_sel_hi:[0,1]
	v_pk_mul_f32 v[8:9], v[8:9], v[30:31] op_sel_hi:[0,1]
	v_cvt_pk_bf16_f32 v4, v4, v5
	v_cvt_pk_bf16_f32 v5, v6, v7
	v_cvt_pk_bf16_f32 v6, v8, v9
	v_mul_f32_e32 v8, 0x3b800000, v1
	v_cvt_pk_bf16_f32 v7, v12, v13
	global_store_dwordx4 v[10:11], v[4:7], off offset:256
	v_lshl_add_u64 v[10:11], v[2:3], 0, s[16:17]
	v_add_co_u32_e32 v2, vcc, s55, v2
	v_pk_mul_f32 v[4:5], v[8:9], v[34:35] op_sel_hi:[0,1]
	v_pk_mul_f32 v[6:7], v[8:9], v[36:37] op_sel_hi:[0,1]
	v_cvt_pk_bf16_f32 v4, v4, v5
	v_cvt_pk_bf16_f32 v5, v6, v7
	v_addc_co_u32_e32 v3, vcc, 0, v3, vcc
	v_pk_mul_f32 v[12:13], v[8:9], v[28:29] op_sel_hi:[0,1]
	v_pk_mul_f32 v[14:15], v[8:9], v[26:27] op_sel_hi:[0,1]
	v_cvt_pk_bf16_f32 v6, v14, v15
	v_cvt_pk_bf16_f32 v7, v12, v13
	global_store_dwordx4 v[2:3], v[4:7], off
	v_pk_mul_f32 v[2:3], v[8:9], v[22:23] op_sel_hi:[0,1]
	s_andn2_b64 vcc, exec, s[0:1]
	v_pk_mul_f32 v[4:5], v[8:9], v[24:25] op_sel_hi:[0,1]
	s_mov_b64 s[0:1], -1
	v_pk_mul_f32 v[6:7], v[8:9], v[20:21] op_sel_hi:[0,1]
	v_pk_mul_f32 v[8:9], v[8:9], v[18:19] op_sel_hi:[0,1]
	v_cvt_pk_bf16_f32 v2, v2, v3
	v_cvt_pk_bf16_f32 v3, v4, v5
	v_cvt_pk_bf16_f32 v4, v8, v9
	v_cvt_pk_bf16_f32 v5, v6, v7
	global_store_dwordx4 v[10:11], v[2:5], off offset:256
	s_cbranch_vccnz .LBB0_1120
	s_nop 0
	v_lshl_add_u32 v2, s18, 8, v172
	v_ashrrev_i32_e32 v3, 31, v2
	v_lshl_add_u64 v[2:3], v[2:3], 2, s[4:5]
	global_load_dword v154, v[2:3], off
	global_load_dword v183, v[2:3], off offset:64
	global_load_dword v182, v[2:3], off offset:128
	global_load_dword v181, v[2:3], off offset:192
	global_load_dword v180, v[2:3], off offset:512
	global_load_dword v179, v[2:3], off offset:576
	global_load_dword v173, v[2:3], off offset:640
	global_load_dword v1, v[2:3], off offset:704
	s_mov_b64 s[0:1], 0
	s_branch .LBB0_1120
